# GEMM main loops: per-segment s_setprio toggles removed (priority stays 0)
# baseline (speedup 1.0000x reference)
; #define PG8_STAGE(bufoff, gbase, voff) do { _Pragma("unroll") for (int _i = 0; _i < 2; ++_i) \
;         __builtin_amdgcn_global_load_lds((const unsigned*)((const char*)(gbase) + (voff)[_i]), (PG8_LAS unsigned*)(lds + (bufoff) + ldsw + _i * 8192), 16, 0, 0); } while (0)
; #define PG8_LDA(dst, b, h) do { _Pragma("unroll") for (int m = 0; m < 4; ++m) _Pragma("unroll") for (int k = 0; k < 2; ++k) dst[m][k] = *(const PG8_LAS bf16x8*)(lds + PG8_SA(b, h) + aoff + m * 2048 + k * 1024); } while (0)
; #define PG8_LDB(dst, b, h) do { _Pragma("unroll") for (int n = 0; n < 2; ++n) _Pragma("unroll") for (int k = 0; k < 2; ++k) dst[n][k] = *(const PG8_LAS bf16x8*)(lds + PG8_SB(b, h) + boff + n * 2048 + k * 1024); } while (0)
; #define PG8_MMA(ai, bj, At, Bt) do { __builtin_amdgcn_s_setprio(1); _Pragma("unroll") for (int m = 0; m < 4; ++m) _Pragma("unroll") for (int n = 0; n < 2; ++n) _Pragma("unroll") for (int k = 0; k < 2; ++k) \
;         acc[ai][bj][m][n] = __builtin_amdgcn_mfma_f32_16x16x32_bf16(Bt[n][k], At[m][k], acc[ai][bj][m][n], 0, 0, 0); __builtin_amdgcn_s_setprio(0); } while (0)
; #define PG8_WAIT_V(n) asm volatile("s_waitcnt vmcnt(" #n ")" ::: "memory")
; #define PG8_BAR __builtin_amdgcn_s_barrier()
; template <class Epi, class Sched, bool ALIGN_EPI = false, bool SP2 = false>
; __device__ __forceinline__ void gemm_phase(PG8_LAS unsigned char* lds, const Gemm g, const Sched& S, const Epi& E) {
;     ...
;         for (int t = 0; t < nt; t += 2) {
;             const bool last = (t == nt - 2);
;             const char* a1 = cA + (size_t)(t + 1) * kstep;
;             const char* a2 = last ? nA : cA + (size_t)(t + 2) * kstep; const char* b2 = last ? nB : cB + (size_t)(t + 2) * kstep;
;             const char* a3 = a2 + kstep; const char* b3 = b2 + kstep;
;             if (last && has_next) S.a_ready(nxt);
;             if constexpr (SP2) {
;             PG8_LDB(B0, 0, 0); PG8_LDB(B1, 0, 1); PG8_SCHED; PG8_LDA(At, 0, 0); PG8_STAGE(PG8_SA(1, 1), a1 + hstep, voffA);
;             PG8_WAIT_V(8); PG8_WAIT_L(0); PG8_BAR; PG8_MMA(0, 0, At, B0); PG8_MMA(0, 1, At, B1); PG8_BAR; PG8_SCHED;
;             PG8_LDA(At, 0, 1); PG8_STAGE(PG8_SB(0, 0), b2, voffB); PG8_STAGE(PG8_SB(0, 1), b2 + hstep, voffB); PG8_STAGE(PG8_SA(0, 0), a2, voffA);
;             PG8_WAIT_V(8); PG8_WAIT_L(0); PG8_BAR; PG8_MMA(1, 0, At, B0); PG8_MMA(1, 1, At, B1); PG8_BAR; PG8_SCHED;
.LBB0_120:
	ds_read_b128 v[154:157], v150
	ds_read_b128 v[158:161], v150 offset:1024
	ds_read_b128 v[162:165], v150 offset:2048
	ds_read_b128 v[166:169], v150 offset:3072
	ds_read_b128 v[170:173], v151
	ds_read_b128 v[174:177], v151 offset:1024
	ds_read_b128 v[178:181], v151 offset:2048
	ds_read_b128 v[184:187], v151 offset:3072
	s_add_u32 s22, s42, 0xfffc0080
	s_addc_u32 s23, s43, -1
	s_cmp_eq_u32 s65, 12
	s_cselect_b32 s23, s6, s23
	s_cselect_b32 s22, s19, s22
	s_cselect_b32 s55, s17, s64
	s_cselect_b32 s54, s62, s63
	v_lshl_add_u64 v[146:147], s[42:43], 0, v[138:139]
	s_add_i32 m0, s31, 0xc000
	ds_read_b128 v[188:191], v152
	ds_read_b128 v[192:195], v152 offset:1024
	ds_read_b128 v[196:199], v152 offset:2048
	ds_read_b128 v[200:203], v152 offset:3072
	ds_read_b128 v[204:207], v152 offset:4096
	ds_read_b128 v[208:211], v152 offset:5120
	ds_read_b128 v[212:215], v152 offset:6144
	ds_read_b128 v[216:219], v152 offset:7168
	global_load_lds_dwordx4 v[146:147], off
	v_lshl_add_u64 v[146:147], s[42:43], 0, v[140:141]
	s_add_i32 m0, s31, 0xe000
	s_nop 0
	global_load_lds_dwordx4 v[146:147], off
	s_waitcnt vmcnt(8)
	s_waitcnt lgkmcnt(0)
	s_barrier
	s_waitcnt lgkmcnt(0)
	v_mfma_f32_16x16x32_bf16 v[126:129], v[154:157], v[188:191], v[126:129]
	v_mfma_f32_16x16x32_bf16 v[122:125], v[162:165], v[188:191], v[122:125]
	v_mfma_f32_16x16x32_bf16 v[118:121], v[154:157], v[196:199], v[118:121]
	v_mfma_f32_16x16x32_bf16 v[110:113], v[162:165], v[196:199], v[110:113]
	v_mfma_f32_16x16x32_bf16 v[102:105], v[154:157], v[204:207], v[102:105]
	v_mfma_f32_16x16x32_bf16 v[94:97], v[162:165], v[204:207], v[94:97]
	v_mfma_f32_16x16x32_bf16 v[86:89], v[154:157], v[212:215], v[86:89]
	v_mfma_f32_16x16x32_bf16 v[78:81], v[162:165], v[212:215], v[78:81]
	v_mfma_f32_16x16x32_bf16 v[126:129], v[158:161], v[192:195], v[126:129]
	v_mfma_f32_16x16x32_bf16 v[122:125], v[166:169], v[192:195], v[122:125]
	v_mfma_f32_16x16x32_bf16 v[118:121], v[158:161], v[200:203], v[118:121]
	v_mfma_f32_16x16x32_bf16 v[110:113], v[166:169], v[200:203], v[110:113]
	v_mfma_f32_16x16x32_bf16 v[102:105], v[158:161], v[208:211], v[102:105]
	v_mfma_f32_16x16x32_bf16 v[94:97], v[166:169], v[208:211], v[94:97]
	v_mfma_f32_16x16x32_bf16 v[86:89], v[158:161], v[216:219], v[86:89]
	v_mfma_f32_16x16x32_bf16 v[78:81], v[166:169], v[216:219], v[78:81]
	v_mfma_f32_16x16x32_bf16 v[114:117], v[170:173], v[188:191], v[114:117]
	v_mfma_f32_16x16x32_bf16 v[106:109], v[178:181], v[188:191], v[106:109]
	v_mfma_f32_16x16x32_bf16 v[98:101], v[170:173], v[196:199], v[98:101]
	v_mfma_f32_16x16x32_bf16 v[90:93], v[178:181], v[196:199], v[90:93]
	v_mfma_f32_16x16x32_bf16 v[82:85], v[170:173], v[204:207], v[82:85]
	v_mfma_f32_16x16x32_bf16 v[74:77], v[178:181], v[204:207], v[74:77]
	v_mfma_f32_16x16x32_bf16 v[70:73], v[170:173], v[212:215], v[70:73]
	v_mfma_f32_16x16x32_bf16 v[66:69], v[178:181], v[212:215], v[66:69]
	v_mfma_f32_16x16x32_bf16 v[114:117], v[174:177], v[192:195], v[114:117]
	v_mfma_f32_16x16x32_bf16 v[106:109], v[184:187], v[192:195], v[106:109]
	v_mfma_f32_16x16x32_bf16 v[98:101], v[174:177], v[200:203], v[98:101]
	v_mfma_f32_16x16x32_bf16 v[90:93], v[184:187], v[200:203], v[90:93]
	v_mfma_f32_16x16x32_bf16 v[82:85], v[174:177], v[208:211], v[82:85]
	v_mfma_f32_16x16x32_bf16 v[74:77], v[184:187], v[208:211], v[74:77]
	v_mfma_f32_16x16x32_bf16 v[70:73], v[174:177], v[216:219], v[70:73]
	v_mfma_f32_16x16x32_bf16 v[66:69], v[184:187], v[216:219], v[66:69]
	s_barrier
	s_add_i32 s66, s58, s28
	v_lshl_add_u64 v[146:147], s[54:55], 0, v[132:133]
	s_mov_b32 m0, s66
	ds_read_b128 v[188:191], v152 offset:16384
	ds_read_b128 v[192:195], v152 offset:17408
	ds_read_b128 v[196:199], v152 offset:18432
	ds_read_b128 v[200:203], v152 offset:19456
	ds_read_b128 v[204:207], v152 offset:20480
	ds_read_b128 v[208:211], v152 offset:21504
	ds_read_b128 v[212:215], v152 offset:22528
	ds_read_b128 v[216:219], v152 offset:23552
	global_load_lds_dwordx4 v[146:147], off
	s_add_i32 m0, s66, 0x2000
	s_add_u32 s66, s54, 0x40000
	v_lshl_add_u64 v[220:221], s[54:55], 0, v[136:137]
	s_addc_u32 s67, s55, 0
	s_add_i32 s68, s59, s28
	global_load_lds_dwordx4 v[220:221], off
	v_lshl_add_u64 v[222:223], s[66:67], 0, v[132:133]
	s_mov_b32 m0, s68
	v_lshl_add_u64 v[224:225], s[22:23], 0, v[134:135]
	global_load_lds_dwordx4 v[222:223], off
	v_lshl_add_u64 v[222:223], s[66:67], 0, v[136:137]
	s_add_i32 m0, s68, 0x2000
	s_nop 0
	global_load_lds_dwordx4 v[222:223], off
	v_lshl_add_u64 v[222:223], s[22:23], 0, v[130:131]
	s_mov_b32 m0, s31
	s_nop 0
	global_load_lds_dwordx4 v[222:223], off
	s_mov_b32 m0, s33
	s_nop 0
	global_load_lds_dwordx4 v[224:225], off
	s_waitcnt vmcnt(8)
	s_waitcnt lgkmcnt(0)
	s_barrier
; #define PG8_STAGE(bufoff, gbase, voff) do { _Pragma("unroll") for (int _i = 0; _i < 2; ++_i) \
;         __builtin_amdgcn_global_load_lds((const unsigned*)((const char*)(gbase) + (voff)[_i]), (PG8_LAS unsigned*)(lds + (bufoff) + ldsw + _i * 8192), 16, 0, 0); } while (0)
; #define PG8_LDA(dst, b, h) do { _Pragma("unroll") for (int m = 0; m < 4; ++m) _Pragma("unroll") for (int k = 0; k < 2; ++k) dst[m][k] = *(const PG8_LAS bf16x8*)(lds + PG8_SA(b, h) + aoff + m * 2048 + k * 1024); } while (0)
; #define PG8_LDB(dst, b, h) do { _Pragma("unroll") for (int n = 0; n < 2; ++n) _Pragma("unroll") for (int k = 0; k < 2; ++k) dst[n][k] = *(const PG8_LAS bf16x8*)(lds + PG8_SB(b, h) + boff + n * 2048 + k * 1024); } while (0)
; #define PG8_MMA(ai, bj, At, Bt) do { __builtin_amdgcn_s_setprio(1); _Pragma("unroll") for (int m = 0; m < 4; ++m) _Pragma("unroll") for (int n = 0; n < 2; ++n) _Pragma("unroll") for (int k = 0; k < 2; ++k) \
;         acc[ai][bj][m][n] = __builtin_amdgcn_mfma_f32_16x16x32_bf16(Bt[n][k], At[m][k], acc[ai][bj][m][n], 0, 0, 0); __builtin_amdgcn_s_setprio(0); } while (0)
; #define PG8_WAIT_V(n) asm volatile("s_waitcnt vmcnt(" #n ")" ::: "memory")
; #define PG8_WAIT_L(n) asm volatile("s_waitcnt lgkmcnt(" #n ")" ::: "memory")
; #define PG8_BAR __builtin_amdgcn_s_barrier()
; #define PG8_SCHED __builtin_amdgcn_sched_barrier(0)
; template <class Epi, class Sched, bool ALIGN_EPI = false, bool SP2 = false>
; __device__ __forceinline__ void gemm_phase(PG8_LAS unsigned char* lds, const Gemm g, const Sched& S, const Epi& E) {
;     ...
;             PG8_WAIT_V(8); PG8_WAIT_L(0); PG8_BAR; PG8_MMA(1, 0, At, B0); PG8_MMA(1, 1, At, B1); PG8_BAR; PG8_SCHED;
;             PG8_LDB(B0, 1, 0); PG8_LDB(B1, 1, 1); PG8_SCHED; PG8_LDA(At, 1, 0); PG8_STAGE(PG8_SA(0, 1), a2 + hstep, voffA);
;             PG8_WAIT_V(8); PG8_WAIT_L(0); PG8_BAR; PG8_MMA(0, 0, At, B0); PG8_MMA(0, 1, At, B1); PG8_BAR; PG8_SCHED;
	s_waitcnt lgkmcnt(0)
	v_mfma_f32_16x16x32_bf16 v[62:65], v[154:157], v[188:191], v[62:65]
	v_mfma_f32_16x16x32_bf16 v[58:61], v[162:165], v[188:191], v[58:61]
	v_mfma_f32_16x16x32_bf16 v[54:57], v[154:157], v[196:199], v[54:57]
	v_mfma_f32_16x16x32_bf16 v[46:49], v[162:165], v[196:199], v[46:49]
	v_mfma_f32_16x16x32_bf16 v[38:41], v[154:157], v[204:207], v[38:41]
	v_mfma_f32_16x16x32_bf16 v[30:33], v[162:165], v[204:207], v[30:33]
	v_mfma_f32_16x16x32_bf16 v[22:25], v[154:157], v[212:215], v[22:25]
	v_mfma_f32_16x16x32_bf16 v[14:17], v[162:165], v[212:215], v[14:17]
	v_mfma_f32_16x16x32_bf16 v[62:65], v[158:161], v[192:195], v[62:65]
	v_mfma_f32_16x16x32_bf16 v[58:61], v[166:169], v[192:195], v[58:61]
	v_mfma_f32_16x16x32_bf16 v[54:57], v[158:161], v[200:203], v[54:57]
	v_mfma_f32_16x16x32_bf16 v[46:49], v[166:169], v[200:203], v[46:49]
	v_mfma_f32_16x16x32_bf16 v[38:41], v[158:161], v[208:211], v[38:41]
	v_mfma_f32_16x16x32_bf16 v[30:33], v[166:169], v[208:211], v[30:33]
	v_mfma_f32_16x16x32_bf16 v[22:25], v[158:161], v[216:219], v[22:25]
	v_mfma_f32_16x16x32_bf16 v[14:17], v[166:169], v[216:219], v[14:17]
	v_mfma_f32_16x16x32_bf16 v[50:53], v[170:173], v[188:191], v[50:53]
	v_mfma_f32_16x16x32_bf16 v[42:45], v[178:181], v[188:191], v[42:45]
	v_mfma_f32_16x16x32_bf16 v[34:37], v[170:173], v[196:199], v[34:37]
	v_mfma_f32_16x16x32_bf16 v[26:29], v[178:181], v[196:199], v[26:29]
	v_mfma_f32_16x16x32_bf16 v[18:21], v[170:173], v[204:207], v[18:21]
	v_mfma_f32_16x16x32_bf16 v[10:13], v[178:181], v[204:207], v[10:13]
	v_mfma_f32_16x16x32_bf16 v[6:9], v[170:173], v[212:215], v[6:9]
	v_mfma_f32_16x16x32_bf16 v[2:5], v[178:181], v[212:215], v[2:5]
	v_mfma_f32_16x16x32_bf16 v[50:53], v[174:177], v[192:195], v[50:53]
	v_mfma_f32_16x16x32_bf16 v[42:45], v[184:187], v[192:195], v[42:45]
	v_mfma_f32_16x16x32_bf16 v[34:37], v[174:177], v[200:203], v[34:37]
	v_mfma_f32_16x16x32_bf16 v[26:29], v[184:187], v[200:203], v[26:29]
	v_mfma_f32_16x16x32_bf16 v[18:21], v[174:177], v[208:211], v[18:21]
	v_mfma_f32_16x16x32_bf16 v[10:13], v[184:187], v[208:211], v[10:13]
	v_mfma_f32_16x16x32_bf16 v[6:9], v[174:177], v[216:219], v[6:9]
	v_mfma_f32_16x16x32_bf16 v[2:5], v[184:187], v[216:219], v[2:5]
	s_barrier
	s_add_i32 s66, 0, 0x18000
	v_add_u32_e32 v153, s66, v148
	s_add_i32 s67, 0, 0x1c000
	ds_read_b128 v[154:157], v153
	ds_read_b128 v[158:161], v153 offset:1024
	ds_read_b128 v[162:165], v153 offset:2048
	ds_read_b128 v[166:169], v153 offset:3072
	v_add_u32_e32 v153, s67, v148
	ds_read_b128 v[170:173], v153
	ds_read_b128 v[174:177], v153 offset:1024
	ds_read_b128 v[178:181], v153 offset:2048
	ds_read_b128 v[184:187], v153 offset:3072
	s_add_u32 s22, s22, 0x40000
	s_addc_u32 s23, s23, 0
	s_mov_b32 m0, s34
	v_lshl_add_u64 v[226:227], s[22:23], 0, v[130:131]
	ds_read_b128 v[188:191], v152 offset:32768
	ds_read_b128 v[192:195], v152 offset:33792
	ds_read_b128 v[196:199], v152 offset:34816
	ds_read_b128 v[200:203], v152 offset:35840
	ds_read_b128 v[204:207], v152 offset:36864
	ds_read_b128 v[208:211], v152 offset:37888
	ds_read_b128 v[212:215], v152 offset:38912
	ds_read_b128 v[216:219], v152 offset:39936
	global_load_lds_dwordx4 v[226:227], off
	v_lshl_add_u64 v[226:227], s[22:23], 0, v[134:135]
	s_mov_b32 m0, s35
	s_nop 0
	global_load_lds_dwordx4 v[226:227], off
	s_waitcnt vmcnt(8)
	s_waitcnt lgkmcnt(0)
	s_barrier
	s_waitcnt lgkmcnt(0)
	v_mfma_f32_16x16x32_bf16 v[126:129], v[154:157], v[188:191], v[126:129]
	v_mfma_f32_16x16x32_bf16 v[122:125], v[162:165], v[188:191], v[122:125]
	v_mfma_f32_16x16x32_bf16 v[118:121], v[154:157], v[196:199], v[118:121]
	v_mfma_f32_16x16x32_bf16 v[110:113], v[162:165], v[196:199], v[110:113]
	v_mfma_f32_16x16x32_bf16 v[102:105], v[154:157], v[204:207], v[102:105]
	v_mfma_f32_16x16x32_bf16 v[94:97], v[162:165], v[204:207], v[94:97]
	v_mfma_f32_16x16x32_bf16 v[86:89], v[154:157], v[212:215], v[86:89]
	v_mfma_f32_16x16x32_bf16 v[78:81], v[162:165], v[212:215], v[78:81]
	v_mfma_f32_16x16x32_bf16 v[126:129], v[158:161], v[192:195], v[126:129]
	v_mfma_f32_16x16x32_bf16 v[122:125], v[166:169], v[192:195], v[122:125]
	v_mfma_f32_16x16x32_bf16 v[118:121], v[158:161], v[200:203], v[118:121]
	v_mfma_f32_16x16x32_bf16 v[110:113], v[166:169], v[200:203], v[110:113]
	v_mfma_f32_16x16x32_bf16 v[102:105], v[158:161], v[208:211], v[102:105]
	v_mfma_f32_16x16x32_bf16 v[94:97], v[166:169], v[208:211], v[94:97]
	v_mfma_f32_16x16x32_bf16 v[86:89], v[158:161], v[216:219], v[86:89]
	v_mfma_f32_16x16x32_bf16 v[78:81], v[166:169], v[216:219], v[78:81]
	v_mfma_f32_16x16x32_bf16 v[114:117], v[170:173], v[188:191], v[114:117]
	v_mfma_f32_16x16x32_bf16 v[106:109], v[178:181], v[188:191], v[106:109]
	v_mfma_f32_16x16x32_bf16 v[98:101], v[170:173], v[196:199], v[98:101]
	v_mfma_f32_16x16x32_bf16 v[90:93], v[178:181], v[196:199], v[90:93]
	v_mfma_f32_16x16x32_bf16 v[82:85], v[170:173], v[204:207], v[82:85]
	v_mfma_f32_16x16x32_bf16 v[74:77], v[178:181], v[204:207], v[74:77]
	v_mfma_f32_16x16x32_bf16 v[70:73], v[170:173], v[212:215], v[70:73]
	v_mfma_f32_16x16x32_bf16 v[66:69], v[178:181], v[212:215], v[66:69]
	v_mfma_f32_16x16x32_bf16 v[114:117], v[174:177], v[192:195], v[114:117]
	v_mfma_f32_16x16x32_bf16 v[106:109], v[184:187], v[192:195], v[106:109]
	v_mfma_f32_16x16x32_bf16 v[98:101], v[174:177], v[200:203], v[98:101]
	v_mfma_f32_16x16x32_bf16 v[90:93], v[184:187], v[200:203], v[90:93]
	v_mfma_f32_16x16x32_bf16 v[82:85], v[174:177], v[208:211], v[82:85]
	v_mfma_f32_16x16x32_bf16 v[74:77], v[184:187], v[208:211], v[74:77]
	v_mfma_f32_16x16x32_bf16 v[70:73], v[174:177], v[216:219], v[70:73]
	v_mfma_f32_16x16x32_bf16 v[66:69], v[184:187], v[216:219], v[66:69]
	s_barrier
; #define PG8_STAGE(bufoff, gbase, voff) do { _Pragma("unroll") for (int _i = 0; _i < 2; ++_i) \
;         __builtin_amdgcn_global_load_lds((const unsigned*)((const char*)(gbase) + (voff)[_i]), (PG8_LAS unsigned*)(lds + (bufoff) + ldsw + _i * 8192), 16, 0, 0); } while (0)
; #define PG8_LDA(dst, b, h) do { _Pragma("unroll") for (int m = 0; m < 4; ++m) _Pragma("unroll") for (int k = 0; k < 2; ++k) dst[m][k] = *(const PG8_LAS bf16x8*)(lds + PG8_SA(b, h) + aoff + m * 2048 + k * 1024); } while (0)
; #define PG8_MMA(ai, bj, At, Bt) do { __builtin_amdgcn_s_setprio(1); _Pragma("unroll") for (int m = 0; m < 4; ++m) _Pragma("unroll") for (int n = 0; n < 2; ++n) _Pragma("unroll") for (int k = 0; k < 2; ++k) \
;         acc[ai][bj][m][n] = __builtin_amdgcn_mfma_f32_16x16x32_bf16(Bt[n][k], At[m][k], acc[ai][bj][m][n], 0, 0, 0); __builtin_amdgcn_s_setprio(0); } while (0)
; #define PG8_WAIT_V(n) asm volatile("s_waitcnt vmcnt(" #n ")" ::: "memory")
; #define PG8_WAIT_L(n) asm volatile("s_waitcnt lgkmcnt(" #n ")" ::: "memory")
; #define PG8_BAR __builtin_amdgcn_s_barrier()
; #define PG8_SCHED __builtin_amdgcn_sched_barrier(0)
; template <class Epi, class Sched, bool ALIGN_EPI = false, bool SP2 = false>
; __device__ __forceinline__ void gemm_phase(PG8_LAS unsigned char* lds, const Gemm g, const Sched& S, const Epi& E) {
;     ...
;         for (int t = 0; t < nt; t += 2) {
;     ...
;             PG8_LDA(At, 1, 1); PG8_STAGE(PG8_SB(1, 0), b3, voffB); PG8_STAGE(PG8_SB(1, 1), b3 + hstep, voffB); PG8_STAGE(PG8_SA(1, 0), a3, voffA);
;             PG8_WAIT_V(8); PG8_WAIT_L(0); PG8_BAR; PG8_MMA(1, 0, At, B0); PG8_MMA(1, 1, At, B1); PG8_BAR; PG8_SCHED;
	s_add_i32 s22, s66, s28
	v_lshl_add_u64 v[146:147], v[146:147], 0, s[12:13]
	s_mov_b32 m0, s22
	ds_read_b128 v[188:191], v152 offset:49152
	ds_read_b128 v[192:195], v152 offset:50176
	ds_read_b128 v[196:199], v152 offset:51200
	ds_read_b128 v[200:203], v152 offset:52224
	ds_read_b128 v[204:207], v152 offset:53248
	ds_read_b128 v[208:211], v152 offset:54272
	ds_read_b128 v[212:215], v152 offset:55296
	ds_read_b128 v[216:219], v152 offset:56320
	global_load_lds_dwordx4 v[146:147], off
	s_add_i32 m0, s22, 0x2000
	s_add_u32 s22, s54, 0x40080
	v_lshl_add_u64 v[146:147], v[220:221], 0, s[12:13]
	s_addc_u32 s23, s55, 0
	s_add_i32 s54, s67, s28
	global_load_lds_dwordx4 v[146:147], off
	v_lshl_add_u64 v[146:147], s[22:23], 0, v[132:133]
	s_mov_b32 m0, s54
	s_nop 0
	global_load_lds_dwordx4 v[146:147], off
	v_lshl_add_u64 v[146:147], s[22:23], 0, v[136:137]
	s_add_i32 m0, s54, 0x2000
	s_nop 0
	global_load_lds_dwordx4 v[146:147], off
	v_lshl_add_u64 v[146:147], v[222:223], 0, s[12:13]
	s_mov_b32 m0, s56
	s_nop 0
	global_load_lds_dwordx4 v[146:147], off
	v_lshl_add_u64 v[146:147], v[224:225], 0, s[12:13]
	s_mov_b32 m0, s57
	s_nop 0
	global_load_lds_dwordx4 v[146:147], off
	s_waitcnt vmcnt(8)
	s_waitcnt lgkmcnt(0)
	s_barrier
	s_waitcnt lgkmcnt(0)
	v_mfma_f32_16x16x32_bf16 v[62:65], v[154:157], v[188:191], v[62:65]
	v_mfma_f32_16x16x32_bf16 v[58:61], v[162:165], v[188:191], v[58:61]
	v_mfma_f32_16x16x32_bf16 v[54:57], v[154:157], v[196:199], v[54:57]
	v_mfma_f32_16x16x32_bf16 v[46:49], v[162:165], v[196:199], v[46:49]
	v_mfma_f32_16x16x32_bf16 v[38:41], v[154:157], v[204:207], v[38:41]
	v_mfma_f32_16x16x32_bf16 v[30:33], v[162:165], v[204:207], v[30:33]
	v_mfma_f32_16x16x32_bf16 v[22:25], v[154:157], v[212:215], v[22:25]
	v_mfma_f32_16x16x32_bf16 v[14:17], v[162:165], v[212:215], v[14:17]
	v_mfma_f32_16x16x32_bf16 v[62:65], v[158:161], v[192:195], v[62:65]
	v_mfma_f32_16x16x32_bf16 v[58:61], v[166:169], v[192:195], v[58:61]
	v_mfma_f32_16x16x32_bf16 v[54:57], v[158:161], v[200:203], v[54:57]
	v_mfma_f32_16x16x32_bf16 v[46:49], v[166:169], v[200:203], v[46:49]
	v_mfma_f32_16x16x32_bf16 v[38:41], v[158:161], v[208:211], v[38:41]
	v_mfma_f32_16x16x32_bf16 v[30:33], v[166:169], v[208:211], v[30:33]
	v_mfma_f32_16x16x32_bf16 v[22:25], v[158:161], v[216:219], v[22:25]
	v_mfma_f32_16x16x32_bf16 v[14:17], v[166:169], v[216:219], v[14:17]
	v_mfma_f32_16x16x32_bf16 v[50:53], v[170:173], v[188:191], v[50:53]
	v_mfma_f32_16x16x32_bf16 v[42:45], v[178:181], v[188:191], v[42:45]
	v_mfma_f32_16x16x32_bf16 v[34:37], v[170:173], v[196:199], v[34:37]
	v_mfma_f32_16x16x32_bf16 v[26:29], v[178:181], v[196:199], v[26:29]
	v_mfma_f32_16x16x32_bf16 v[18:21], v[170:173], v[204:207], v[18:21]
	v_mfma_f32_16x16x32_bf16 v[10:13], v[178:181], v[204:207], v[10:13]
	v_mfma_f32_16x16x32_bf16 v[6:9], v[170:173], v[212:215], v[6:9]
	v_mfma_f32_16x16x32_bf16 v[2:5], v[178:181], v[212:215], v[2:5]
	v_mfma_f32_16x16x32_bf16 v[50:53], v[174:177], v[192:195], v[50:53]
	v_mfma_f32_16x16x32_bf16 v[42:45], v[184:187], v[192:195], v[42:45]
	v_mfma_f32_16x16x32_bf16 v[34:37], v[174:177], v[200:203], v[34:37]
	v_mfma_f32_16x16x32_bf16 v[26:29], v[184:187], v[200:203], v[26:29]
	v_mfma_f32_16x16x32_bf16 v[18:21], v[174:177], v[208:211], v[18:21]
	v_mfma_f32_16x16x32_bf16 v[10:13], v[184:187], v[208:211], v[10:13]
	v_mfma_f32_16x16x32_bf16 v[6:9], v[174:177], v[216:219], v[6:9]
	v_mfma_f32_16x16x32_bf16 v[2:5], v[184:187], v[216:219], v[2:5]
	s_barrier
	s_add_i32 s65, s65, 2
	s_add_u32 s42, s42, 0x100
	s_addc_u32 s43, s43, 0
	s_add_u32 s63, s63, 0x100
	s_addc_u32 s64, s64, 0
	s_cmp_gt_u32 s65, 13
	s_cbranch_scc0 .LBB0_120
	s_and_b64 vcc, exec, s[14:15]
	s_cbranch_vccz .LBB0_123
	s_barrier

; #define PG8_STAGE(bufoff, gbase, voff) do { _Pragma("unroll") for (int _i = 0; _i < 2; ++_i) \
;         __builtin_amdgcn_global_load_lds((const unsigned*)((const char*)(gbase) + (voff)[_i]), (PG8_LAS unsigned*)(lds + (bufoff) + ldsw + _i * 8192), 16, 0, 0); } while (0)
; #define PG8_LDA(dst, b, h) do { _Pragma("unroll") for (int m = 0; m < 4; ++m) _Pragma("unroll") for (int k = 0; k < 2; ++k) dst[m][k] = *(const PG8_LAS bf16x8*)(lds + PG8_SA(b, h) + aoff + m * 2048 + k * 1024); } while (0)
; #define PG8_LDB(dst, b, h) do { _Pragma("unroll") for (int n = 0; n < 2; ++n) _Pragma("unroll") for (int k = 0; k < 2; ++k) dst[n][k] = *(const PG8_LAS bf16x8*)(lds + PG8_SB(b, h) + boff + n * 2048 + k * 1024); } while (0)
; #define PG8_MMA(ai, bj, At, Bt) do { __builtin_amdgcn_s_setprio(1); _Pragma("unroll") for (int m = 0; m < 4; ++m) _Pragma("unroll") for (int n = 0; n < 2; ++n) _Pragma("unroll") for (int k = 0; k < 2; ++k) \
;         acc[ai][bj][m][n] = __builtin_amdgcn_mfma_f32_16x16x32_bf16(Bt[n][k], At[m][k], acc[ai][bj][m][n], 0, 0, 0); __builtin_amdgcn_s_setprio(0); } while (0)
; #define PG8_WAIT_V(n) asm volatile("s_waitcnt vmcnt(" #n ")" ::: "memory")
; #define PG8_WAIT_L(n) asm volatile("s_waitcnt lgkmcnt(" #n ")" ::: "memory")
; #define PG8_BAR __builtin_amdgcn_s_barrier()
; template <class Epi, class Sched, bool ALIGN_EPI = false, bool SP2 = false>
; __device__ __forceinline__ void gemm_phase(PG8_LAS unsigned char* lds, const Gemm g, const Sched& S, const Epi& E) {
;     ...
;             const char* a1 = cA + (size_t)(t + 1) * kstep;
;             const char* a2 = last ? nA : cA + (size_t)(t + 2) * kstep; const char* b2 = last ? nB : cB + (size_t)(t + 2) * kstep;
;             const char* a3 = a2 + kstep; const char* b3 = b2 + kstep;
;             if (last && has_next) S.a_ready(nxt);
;             if constexpr (SP2) {
;             PG8_LDB(B0, 0, 0); PG8_LDB(B1, 0, 1); PG8_SCHED; PG8_LDA(At, 0, 0); PG8_STAGE(PG8_SA(1, 1), a1 + hstep, voffA);
;             PG8_WAIT_V(8); PG8_WAIT_L(0); PG8_BAR; PG8_MMA(0, 0, At, B0); PG8_MMA(0, 1, At, B1); PG8_BAR; PG8_SCHED;
;             PG8_LDA(At, 0, 1); PG8_STAGE(PG8_SB(0, 0), b2, voffB); PG8_STAGE(PG8_SB(0, 1), b2 + hstep, voffB); PG8_STAGE(PG8_SA(0, 0), a2, voffA);
;             PG8_WAIT_V(8); PG8_WAIT_L(0); PG8_BAR; PG8_MMA(1, 0, At, B0); PG8_MMA(1, 1, At, B1); PG8_BAR; PG8_SCHED;
.LBB0_1837:
	ds_read_b128 v[150:153], v138
	ds_read_b128 v[154:157], v138 offset:1024
	ds_read_b128 v[158:161], v138 offset:2048
	ds_read_b128 v[162:165], v138 offset:3072
	ds_read_b128 v[166:169], v139
	ds_read_b128 v[170:173], v139 offset:1024
	ds_read_b128 v[174:177], v139 offset:2048
	ds_read_b128 v[178:181], v139 offset:3072
	s_add_u32 s16, s12, s14
	s_addc_u32 s17, s13, s15
	s_add_u32 s16, s16, 0x1800100
	s_addc_u32 s17, s17, 0
	s_add_u32 s55, s38, s14
	s_addc_u32 s56, s39, s15
	s_cmpk_eq_i32 s14, 0x700
	s_cselect_b32 s19, s7, s17
	s_cselect_b32 s18, s6, s16
	s_cselect_b32 s17, s1, s56
	s_cselect_b32 s16, s0, s55
	s_mov_b32 m0, s43
	v_lshl_add_u64 v[216:217], v[134:135], 0, s[14:15]
	ds_read_b128 v[184:187], v145
	ds_read_b128 v[188:191], v145 offset:1024
	ds_read_b128 v[192:195], v145 offset:2048
	ds_read_b128 v[196:199], v145 offset:3072
	ds_read_b128 v[200:203], v145 offset:4096
	ds_read_b128 v[204:207], v145 offset:5120
	ds_read_b128 v[208:211], v145 offset:6144
	ds_read_b128 v[212:215], v145 offset:7168
	global_load_lds_dwordx4 v[216:217], off
	v_lshl_add_u64 v[216:217], v[136:137], 0, s[14:15]
	s_mov_b32 m0, s44
	s_nop 0
	global_load_lds_dwordx4 v[216:217], off
	s_waitcnt vmcnt(8)
	s_waitcnt lgkmcnt(0)
	s_barrier
	s_waitcnt lgkmcnt(0)
	v_mfma_f32_16x16x32_bf16 v[126:129], v[150:153], v[184:187], v[126:129]
	v_mfma_f32_16x16x32_bf16 v[122:125], v[158:161], v[184:187], v[122:125]
	v_mfma_f32_16x16x32_bf16 v[110:113], v[150:153], v[192:195], v[110:113]
	v_mfma_f32_16x16x32_bf16 v[106:109], v[158:161], v[192:195], v[106:109]
	v_mfma_f32_16x16x32_bf16 v[94:97], v[150:153], v[200:203], v[94:97]
	v_mfma_f32_16x16x32_bf16 v[90:93], v[158:161], v[200:203], v[90:93]
	v_mfma_f32_16x16x32_bf16 v[78:81], v[150:153], v[208:211], v[78:81]
	v_mfma_f32_16x16x32_bf16 v[74:77], v[158:161], v[208:211], v[74:77]
	v_mfma_f32_16x16x32_bf16 v[126:129], v[154:157], v[188:191], v[126:129]
	v_mfma_f32_16x16x32_bf16 v[122:125], v[162:165], v[188:191], v[122:125]
	v_mfma_f32_16x16x32_bf16 v[110:113], v[154:157], v[196:199], v[110:113]
	v_mfma_f32_16x16x32_bf16 v[106:109], v[162:165], v[196:199], v[106:109]
	v_mfma_f32_16x16x32_bf16 v[94:97], v[154:157], v[204:207], v[94:97]
	v_mfma_f32_16x16x32_bf16 v[90:93], v[162:165], v[204:207], v[90:93]
	v_mfma_f32_16x16x32_bf16 v[78:81], v[154:157], v[212:215], v[78:81]
	v_mfma_f32_16x16x32_bf16 v[74:77], v[162:165], v[212:215], v[74:77]
	v_mfma_f32_16x16x32_bf16 v[118:121], v[166:169], v[184:187], v[118:121]
	v_mfma_f32_16x16x32_bf16 v[114:117], v[174:177], v[184:187], v[114:117]
	v_mfma_f32_16x16x32_bf16 v[102:105], v[166:169], v[192:195], v[102:105]
	v_mfma_f32_16x16x32_bf16 v[98:101], v[174:177], v[192:195], v[98:101]
	v_mfma_f32_16x16x32_bf16 v[86:89], v[166:169], v[200:203], v[86:89]
	v_mfma_f32_16x16x32_bf16 v[82:85], v[174:177], v[200:203], v[82:85]
	v_mfma_f32_16x16x32_bf16 v[70:73], v[166:169], v[208:211], v[70:73]
	v_mfma_f32_16x16x32_bf16 v[66:69], v[174:177], v[208:211], v[66:69]
	v_mfma_f32_16x16x32_bf16 v[118:121], v[170:173], v[188:191], v[118:121]
	v_mfma_f32_16x16x32_bf16 v[114:117], v[178:181], v[188:191], v[114:117]
	v_mfma_f32_16x16x32_bf16 v[102:105], v[170:173], v[196:199], v[102:105]
	v_mfma_f32_16x16x32_bf16 v[98:101], v[178:181], v[196:199], v[98:101]
	v_mfma_f32_16x16x32_bf16 v[86:89], v[170:173], v[204:207], v[86:89]
	v_mfma_f32_16x16x32_bf16 v[82:85], v[178:181], v[204:207], v[82:85]
	v_mfma_f32_16x16x32_bf16 v[70:73], v[170:173], v[212:215], v[70:73]
	v_mfma_f32_16x16x32_bf16 v[66:69], v[178:181], v[212:215], v[66:69]
	s_barrier
	s_mov_b32 m0, s45
	v_lshl_add_u64 v[216:217], s[16:17], 0, v[130:131]
	s_add_u32 s56, s16, 0x40000
	ds_read_b128 v[184:187], v145 offset:16384
	ds_read_b128 v[188:191], v145 offset:17408
	ds_read_b128 v[192:195], v145 offset:18432
	ds_read_b128 v[196:199], v145 offset:19456
	ds_read_b128 v[200:203], v145 offset:20480
	ds_read_b128 v[204:207], v145 offset:21504
	ds_read_b128 v[208:211], v145 offset:22528
	ds_read_b128 v[212:215], v145 offset:23552
	global_load_lds_dwordx4 v[216:217], off
	v_lshl_add_u64 v[218:219], s[16:17], 0, v[132:133]
	s_mov_b32 m0, s46
	s_addc_u32 s57, s17, 0
	global_load_lds_dwordx4 v[218:219], off
	v_lshl_add_u64 v[220:221], s[56:57], 0, v[130:131]
	s_mov_b32 m0, s47
	v_lshl_add_u64 v[222:223], s[18:19], 0, v[132:133]
	global_load_lds_dwordx4 v[220:221], off
	v_lshl_add_u64 v[220:221], s[56:57], 0, v[132:133]
	s_mov_b32 m0, s48
	s_nop 0
	global_load_lds_dwordx4 v[220:221], off
	v_lshl_add_u64 v[220:221], s[18:19], 0, v[130:131]
	s_mov_b32 m0, s22
	s_nop 0
	global_load_lds_dwordx4 v[220:221], off
	s_mov_b32 m0, s23
	s_nop 0
	global_load_lds_dwordx4 v[222:223], off
	s_waitcnt vmcnt(8)
	s_waitcnt lgkmcnt(0)
	s_barrier
; #define PG8_STAGE(bufoff, gbase, voff) do { _Pragma("unroll") for (int _i = 0; _i < 2; ++_i) \
;         __builtin_amdgcn_global_load_lds((const unsigned*)((const char*)(gbase) + (voff)[_i]), (PG8_LAS unsigned*)(lds + (bufoff) + ldsw + _i * 8192), 16, 0, 0); } while (0)
; #define PG8_LDA(dst, b, h) do { _Pragma("unroll") for (int m = 0; m < 4; ++m) _Pragma("unroll") for (int k = 0; k < 2; ++k) dst[m][k] = *(const PG8_LAS bf16x8*)(lds + PG8_SA(b, h) + aoff + m * 2048 + k * 1024); } while (0)
; #define PG8_LDB(dst, b, h) do { _Pragma("unroll") for (int n = 0; n < 2; ++n) _Pragma("unroll") for (int k = 0; k < 2; ++k) dst[n][k] = *(const PG8_LAS bf16x8*)(lds + PG8_SB(b, h) + boff + n * 2048 + k * 1024); } while (0)
; #define PG8_MMA(ai, bj, At, Bt) do { __builtin_amdgcn_s_setprio(1); _Pragma("unroll") for (int m = 0; m < 4; ++m) _Pragma("unroll") for (int n = 0; n < 2; ++n) _Pragma("unroll") for (int k = 0; k < 2; ++k) \
;         acc[ai][bj][m][n] = __builtin_amdgcn_mfma_f32_16x16x32_bf16(Bt[n][k], At[m][k], acc[ai][bj][m][n], 0, 0, 0); __builtin_amdgcn_s_setprio(0); } while (0)
; #define PG8_WAIT_V(n) asm volatile("s_waitcnt vmcnt(" #n ")" ::: "memory")
; #define PG8_WAIT_L(n) asm volatile("s_waitcnt lgkmcnt(" #n ")" ::: "memory")
; #define PG8_BAR __builtin_amdgcn_s_barrier()
; #define PG8_SCHED __builtin_amdgcn_sched_barrier(0)
; template <class Epi, class Sched, bool ALIGN_EPI = false, bool SP2 = false>
; __device__ __forceinline__ void gemm_phase(PG8_LAS unsigned char* lds, const Gemm g, const Sched& S, const Epi& E) {
;     ...
;             PG8_WAIT_V(8); PG8_WAIT_L(0); PG8_BAR; PG8_MMA(1, 0, At, B0); PG8_MMA(1, 1, At, B1); PG8_BAR; PG8_SCHED;
;             PG8_LDB(B0, 1, 0); PG8_LDB(B1, 1, 1); PG8_SCHED; PG8_LDA(At, 1, 0); PG8_STAGE(PG8_SA(0, 1), a2 + hstep, voffA);
;             PG8_WAIT_V(8); PG8_WAIT_L(0); PG8_BAR; PG8_MMA(0, 0, At, B0); PG8_MMA(0, 1, At, B1); PG8_BAR; PG8_SCHED;
	s_waitcnt lgkmcnt(0)
	v_mfma_f32_16x16x32_bf16 v[62:65], v[150:153], v[184:187], v[62:65]
	v_mfma_f32_16x16x32_bf16 v[58:61], v[158:161], v[184:187], v[58:61]
	v_mfma_f32_16x16x32_bf16 v[46:49], v[150:153], v[192:195], v[46:49]
	v_mfma_f32_16x16x32_bf16 v[42:45], v[158:161], v[192:195], v[42:45]
	v_mfma_f32_16x16x32_bf16 v[30:33], v[150:153], v[200:203], v[30:33]
	v_mfma_f32_16x16x32_bf16 v[26:29], v[158:161], v[200:203], v[26:29]
	v_mfma_f32_16x16x32_bf16 v[14:17], v[150:153], v[208:211], v[14:17]
	v_mfma_f32_16x16x32_bf16 v[10:13], v[158:161], v[208:211], v[10:13]
	v_mfma_f32_16x16x32_bf16 v[62:65], v[154:157], v[188:191], v[62:65]
	v_mfma_f32_16x16x32_bf16 v[58:61], v[162:165], v[188:191], v[58:61]
	v_mfma_f32_16x16x32_bf16 v[46:49], v[154:157], v[196:199], v[46:49]
	v_mfma_f32_16x16x32_bf16 v[42:45], v[162:165], v[196:199], v[42:45]
	v_mfma_f32_16x16x32_bf16 v[30:33], v[154:157], v[204:207], v[30:33]
	v_mfma_f32_16x16x32_bf16 v[26:29], v[162:165], v[204:207], v[26:29]
	v_mfma_f32_16x16x32_bf16 v[14:17], v[154:157], v[212:215], v[14:17]
	v_mfma_f32_16x16x32_bf16 v[10:13], v[162:165], v[212:215], v[10:13]
	v_mfma_f32_16x16x32_bf16 v[54:57], v[166:169], v[184:187], v[54:57]
	v_mfma_f32_16x16x32_bf16 v[50:53], v[174:177], v[184:187], v[50:53]
	v_mfma_f32_16x16x32_bf16 v[38:41], v[166:169], v[192:195], v[38:41]
	v_mfma_f32_16x16x32_bf16 v[34:37], v[174:177], v[192:195], v[34:37]
	v_mfma_f32_16x16x32_bf16 v[22:25], v[166:169], v[200:203], v[22:25]
	v_mfma_f32_16x16x32_bf16 v[18:21], v[174:177], v[200:203], v[18:21]
	v_mfma_f32_16x16x32_bf16 v[6:9], v[166:169], v[208:211], v[6:9]
	v_mfma_f32_16x16x32_bf16 v[2:5], v[174:177], v[208:211], v[2:5]
	v_mfma_f32_16x16x32_bf16 v[54:57], v[170:173], v[188:191], v[54:57]
	v_mfma_f32_16x16x32_bf16 v[50:53], v[178:181], v[188:191], v[50:53]
	v_mfma_f32_16x16x32_bf16 v[38:41], v[170:173], v[196:199], v[38:41]
	v_mfma_f32_16x16x32_bf16 v[34:37], v[178:181], v[196:199], v[34:37]
	v_mfma_f32_16x16x32_bf16 v[22:25], v[170:173], v[204:207], v[22:25]
	v_mfma_f32_16x16x32_bf16 v[18:21], v[178:181], v[204:207], v[18:21]
	v_mfma_f32_16x16x32_bf16 v[6:9], v[170:173], v[212:215], v[6:9]
	v_mfma_f32_16x16x32_bf16 v[2:5], v[178:181], v[212:215], v[2:5]
	s_barrier
	ds_read_b128 v[150:153], v147
	ds_read_b128 v[154:157], v147 offset:1024
	ds_read_b128 v[158:161], v147 offset:2048
	ds_read_b128 v[162:165], v147 offset:3072
	ds_read_b128 v[166:169], v148
	ds_read_b128 v[170:173], v148 offset:1024
	ds_read_b128 v[174:177], v148 offset:2048
	ds_read_b128 v[178:181], v148 offset:3072
	s_add_u32 s18, s18, 0x40000
	s_addc_u32 s19, s19, 0
	s_mov_b32 m0, s29
	v_lshl_add_u64 v[224:225], s[18:19], 0, v[130:131]
	ds_read_b128 v[184:187], v145 offset:32768
	ds_read_b128 v[188:191], v145 offset:33792
	ds_read_b128 v[192:195], v145 offset:34816
	ds_read_b128 v[196:199], v145 offset:35840
	ds_read_b128 v[200:203], v145 offset:36864
	ds_read_b128 v[204:207], v145 offset:37888
	ds_read_b128 v[208:211], v145 offset:38912
	ds_read_b128 v[212:215], v145 offset:39936
	global_load_lds_dwordx4 v[224:225], off
	v_lshl_add_u64 v[224:225], s[18:19], 0, v[132:133]
	s_mov_b32 m0, s30
	s_nop 0
	global_load_lds_dwordx4 v[224:225], off
	s_waitcnt vmcnt(8)
	s_waitcnt lgkmcnt(0)
	s_barrier
	s_waitcnt lgkmcnt(0)
	v_mfma_f32_16x16x32_bf16 v[126:129], v[150:153], v[184:187], v[126:129]
	v_mfma_f32_16x16x32_bf16 v[122:125], v[158:161], v[184:187], v[122:125]
	v_mfma_f32_16x16x32_bf16 v[110:113], v[150:153], v[192:195], v[110:113]
	v_mfma_f32_16x16x32_bf16 v[106:109], v[158:161], v[192:195], v[106:109]
	v_mfma_f32_16x16x32_bf16 v[94:97], v[150:153], v[200:203], v[94:97]
	v_mfma_f32_16x16x32_bf16 v[90:93], v[158:161], v[200:203], v[90:93]
	v_mfma_f32_16x16x32_bf16 v[78:81], v[150:153], v[208:211], v[78:81]
	v_mfma_f32_16x16x32_bf16 v[74:77], v[158:161], v[208:211], v[74:77]
	v_mfma_f32_16x16x32_bf16 v[126:129], v[154:157], v[188:191], v[126:129]
	v_mfma_f32_16x16x32_bf16 v[122:125], v[162:165], v[188:191], v[122:125]
	v_mfma_f32_16x16x32_bf16 v[110:113], v[154:157], v[196:199], v[110:113]
	v_mfma_f32_16x16x32_bf16 v[106:109], v[162:165], v[196:199], v[106:109]
	v_mfma_f32_16x16x32_bf16 v[94:97], v[154:157], v[204:207], v[94:97]
	v_mfma_f32_16x16x32_bf16 v[90:93], v[162:165], v[204:207], v[90:93]
	v_mfma_f32_16x16x32_bf16 v[78:81], v[154:157], v[212:215], v[78:81]
	v_mfma_f32_16x16x32_bf16 v[74:77], v[162:165], v[212:215], v[74:77]
	v_mfma_f32_16x16x32_bf16 v[118:121], v[166:169], v[184:187], v[118:121]
	v_mfma_f32_16x16x32_bf16 v[114:117], v[174:177], v[184:187], v[114:117]
	v_mfma_f32_16x16x32_bf16 v[102:105], v[166:169], v[192:195], v[102:105]
	v_mfma_f32_16x16x32_bf16 v[98:101], v[174:177], v[192:195], v[98:101]
	v_mfma_f32_16x16x32_bf16 v[86:89], v[166:169], v[200:203], v[86:89]
	v_mfma_f32_16x16x32_bf16 v[82:85], v[174:177], v[200:203], v[82:85]
	v_mfma_f32_16x16x32_bf16 v[70:73], v[166:169], v[208:211], v[70:73]
	v_mfma_f32_16x16x32_bf16 v[66:69], v[174:177], v[208:211], v[66:69]
	v_mfma_f32_16x16x32_bf16 v[118:121], v[170:173], v[188:191], v[118:121]
	v_mfma_f32_16x16x32_bf16 v[114:117], v[178:181], v[188:191], v[114:117]
	v_mfma_f32_16x16x32_bf16 v[102:105], v[170:173], v[196:199], v[102:105]
	v_mfma_f32_16x16x32_bf16 v[98:101], v[178:181], v[196:199], v[98:101]
	v_mfma_f32_16x16x32_bf16 v[86:89], v[170:173], v[204:207], v[86:89]
	v_mfma_f32_16x16x32_bf16 v[82:85], v[178:181], v[204:207], v[82:85]
	v_mfma_f32_16x16x32_bf16 v[70:73], v[170:173], v[212:215], v[70:73]
	v_mfma_f32_16x16x32_bf16 v[66:69], v[178:181], v[212:215], v[66:69]
	s_barrier
; #define PG8_STAGE(bufoff, gbase, voff) do { _Pragma("unroll") for (int _i = 0; _i < 2; ++_i) \
;         __builtin_amdgcn_global_load_lds((const unsigned*)((const char*)(gbase) + (voff)[_i]), (PG8_LAS unsigned*)(lds + (bufoff) + ldsw + _i * 8192), 16, 0, 0); } while (0)
; #define PG8_LDA(dst, b, h) do { _Pragma("unroll") for (int m = 0; m < 4; ++m) _Pragma("unroll") for (int k = 0; k < 2; ++k) dst[m][k] = *(const PG8_LAS bf16x8*)(lds + PG8_SA(b, h) + aoff + m * 2048 + k * 1024); } while (0)
; #define PG8_MMA(ai, bj, At, Bt) do { __builtin_amdgcn_s_setprio(1); _Pragma("unroll") for (int m = 0; m < 4; ++m) _Pragma("unroll") for (int n = 0; n < 2; ++n) _Pragma("unroll") for (int k = 0; k < 2; ++k) \
;         acc[ai][bj][m][n] = __builtin_amdgcn_mfma_f32_16x16x32_bf16(Bt[n][k], At[m][k], acc[ai][bj][m][n], 0, 0, 0); __builtin_amdgcn_s_setprio(0); } while (0)
; #define PG8_WAIT_V(n) asm volatile("s_waitcnt vmcnt(" #n ")" ::: "memory")
; #define PG8_WAIT_L(n) asm volatile("s_waitcnt lgkmcnt(" #n ")" ::: "memory")
; #define PG8_BAR __builtin_amdgcn_s_barrier()
; #define PG8_SCHED __builtin_amdgcn_sched_barrier(0)
; template <class Epi, class Sched, bool ALIGN_EPI = false, bool SP2 = false>
; __device__ __forceinline__ void gemm_phase(PG8_LAS unsigned char* lds, const Gemm g, const Sched& S, const Epi& E) {
;     ...
;         for (int t = 0; t < nt; t += 2) {
;     ...
;             PG8_LDA(At, 1, 1); PG8_STAGE(PG8_SB(1, 0), b3, voffB); PG8_STAGE(PG8_SB(1, 1), b3 + hstep, voffB); PG8_STAGE(PG8_SA(1, 0), a3, voffA);
;             PG8_WAIT_V(8); PG8_WAIT_L(0); PG8_BAR; PG8_MMA(1, 0, At, B0); PG8_MMA(1, 1, At, B1); PG8_BAR; PG8_SCHED;
	s_mov_b32 m0, s49
	v_lshl_add_u64 v[216:217], v[216:217], 0, s[10:11]
	s_add_u32 s16, s16, 0x40080
	ds_read_b128 v[184:187], v145 offset:49152
	ds_read_b128 v[188:191], v145 offset:50176
	ds_read_b128 v[192:195], v145 offset:51200
	ds_read_b128 v[196:199], v145 offset:52224
	ds_read_b128 v[200:203], v145 offset:53248
	ds_read_b128 v[204:207], v145 offset:54272
	ds_read_b128 v[208:211], v145 offset:55296
	ds_read_b128 v[212:215], v145 offset:56320
	global_load_lds_dwordx4 v[216:217], off
	v_lshl_add_u64 v[216:217], v[218:219], 0, s[10:11]
	s_mov_b32 m0, s52
	s_addc_u32 s17, s17, 0
	global_load_lds_dwordx4 v[216:217], off
	v_lshl_add_u64 v[216:217], s[16:17], 0, v[130:131]
	s_mov_b32 m0, s53
	s_nop 0
	global_load_lds_dwordx4 v[216:217], off
	v_lshl_add_u64 v[216:217], s[16:17], 0, v[132:133]
	s_mov_b32 m0, s54
	s_nop 0
	global_load_lds_dwordx4 v[216:217], off
	v_lshl_add_u64 v[216:217], v[220:221], 0, s[10:11]
	s_mov_b32 m0, s34
	s_nop 0
	global_load_lds_dwordx4 v[216:217], off
	v_lshl_add_u64 v[216:217], v[222:223], 0, s[10:11]
	s_mov_b32 m0, s35
	s_nop 0
	global_load_lds_dwordx4 v[216:217], off
	s_waitcnt vmcnt(8)
	s_waitcnt lgkmcnt(0)
	s_barrier
	s_waitcnt lgkmcnt(0)
	v_mfma_f32_16x16x32_bf16 v[62:65], v[150:153], v[184:187], v[62:65]
	v_mfma_f32_16x16x32_bf16 v[58:61], v[158:161], v[184:187], v[58:61]
	v_mfma_f32_16x16x32_bf16 v[46:49], v[150:153], v[192:195], v[46:49]
	v_mfma_f32_16x16x32_bf16 v[42:45], v[158:161], v[192:195], v[42:45]
	v_mfma_f32_16x16x32_bf16 v[30:33], v[150:153], v[200:203], v[30:33]
	v_mfma_f32_16x16x32_bf16 v[26:29], v[158:161], v[200:203], v[26:29]
	v_mfma_f32_16x16x32_bf16 v[14:17], v[150:153], v[208:211], v[14:17]
	v_mfma_f32_16x16x32_bf16 v[10:13], v[158:161], v[208:211], v[10:13]
	v_mfma_f32_16x16x32_bf16 v[62:65], v[154:157], v[188:191], v[62:65]
	v_mfma_f32_16x16x32_bf16 v[58:61], v[162:165], v[188:191], v[58:61]
	v_mfma_f32_16x16x32_bf16 v[46:49], v[154:157], v[196:199], v[46:49]
	v_mfma_f32_16x16x32_bf16 v[42:45], v[162:165], v[196:199], v[42:45]
	v_mfma_f32_16x16x32_bf16 v[30:33], v[154:157], v[204:207], v[30:33]
	v_mfma_f32_16x16x32_bf16 v[26:29], v[162:165], v[204:207], v[26:29]
	v_mfma_f32_16x16x32_bf16 v[14:17], v[154:157], v[212:215], v[14:17]
	v_mfma_f32_16x16x32_bf16 v[10:13], v[162:165], v[212:215], v[10:13]
	v_mfma_f32_16x16x32_bf16 v[54:57], v[166:169], v[184:187], v[54:57]
	v_mfma_f32_16x16x32_bf16 v[50:53], v[174:177], v[184:187], v[50:53]
	v_mfma_f32_16x16x32_bf16 v[38:41], v[166:169], v[192:195], v[38:41]
	v_mfma_f32_16x16x32_bf16 v[34:37], v[174:177], v[192:195], v[34:37]
	v_mfma_f32_16x16x32_bf16 v[22:25], v[166:169], v[200:203], v[22:25]
	v_mfma_f32_16x16x32_bf16 v[18:21], v[174:177], v[200:203], v[18:21]
	v_mfma_f32_16x16x32_bf16 v[6:9], v[166:169], v[208:211], v[6:9]
	v_mfma_f32_16x16x32_bf16 v[2:5], v[174:177], v[208:211], v[2:5]
	v_mfma_f32_16x16x32_bf16 v[54:57], v[170:173], v[188:191], v[54:57]
	v_mfma_f32_16x16x32_bf16 v[50:53], v[178:181], v[188:191], v[50:53]
	v_mfma_f32_16x16x32_bf16 v[38:41], v[170:173], v[196:199], v[38:41]
	v_mfma_f32_16x16x32_bf16 v[34:37], v[178:181], v[196:199], v[34:37]
	v_mfma_f32_16x16x32_bf16 v[22:25], v[170:173], v[204:207], v[22:25]
	v_mfma_f32_16x16x32_bf16 v[18:21], v[178:181], v[204:207], v[18:21]
	v_mfma_f32_16x16x32_bf16 v[6:9], v[170:173], v[212:215], v[6:9]
	v_mfma_f32_16x16x32_bf16 v[2:5], v[178:181], v[212:215], v[2:5]
	s_barrier
	s_add_i32 s42, s42, 2
	s_add_u32 s14, s14, 0x100
	s_addc_u32 s15, s15, 0
	s_cmp_gt_u32 s42, 13
	s_cbranch_scc0 .LBB0_1837
	s_cmpk_lt_u32 s21, 0x100
	s_cbranch_scc0 .LBB0_1840
	s_barrier

; #define PG8_STAGE(bufoff, gbase, voff) do { _Pragma("unroll") for (int _i = 0; _i < 2; ++_i) \
;         __builtin_amdgcn_global_load_lds((const unsigned*)((const char*)(gbase) + (voff)[_i]), (PG8_LAS unsigned*)(lds + (bufoff) + ldsw + _i * 8192), 16, 0, 0); } while (0)
; #define PG8_LDA(dst, b, h) do { _Pragma("unroll") for (int m = 0; m < 4; ++m) _Pragma("unroll") for (int k = 0; k < 2; ++k) dst[m][k] = *(const PG8_LAS bf16x8*)(lds + PG8_SA(b, h) + aoff + m * 2048 + k * 1024); } while (0)
; #define PG8_LDB(dst, b, h) do { _Pragma("unroll") for (int n = 0; n < 2; ++n) _Pragma("unroll") for (int k = 0; k < 2; ++k) dst[n][k] = *(const PG8_LAS bf16x8*)(lds + PG8_SB(b, h) + boff + n * 2048 + k * 1024); } while (0)
; #define PG8_MMA(ai, bj, At, Bt) do { __builtin_amdgcn_s_setprio(1); _Pragma("unroll") for (int m = 0; m < 4; ++m) _Pragma("unroll") for (int n = 0; n < 2; ++n) _Pragma("unroll") for (int k = 0; k < 2; ++k) \
;         acc[ai][bj][m][n] = __builtin_amdgcn_mfma_f32_16x16x32_bf16(Bt[n][k], At[m][k], acc[ai][bj][m][n], 0, 0, 0); __builtin_amdgcn_s_setprio(0); } while (0)
; #define PG8_WAIT_V(n) asm volatile("s_waitcnt vmcnt(" #n ")" ::: "memory")
; #define PG8_BAR __builtin_amdgcn_s_barrier()
; template <class Epi, class Sched, bool ALIGN_EPI = false, bool SP2 = false>
; __device__ __forceinline__ void gemm_phase(PG8_LAS unsigned char* lds, const Gemm g, const Sched& S, const Epi& E) {
;     ...
;         for (int t = 0; t < nt; t += 2) {
;             const bool last = (t == nt - 2);
;             const char* a1 = cA + (size_t)(t + 1) * kstep;
;             const char* a2 = last ? nA : cA + (size_t)(t + 2) * kstep; const char* b2 = last ? nB : cB + (size_t)(t + 2) * kstep;
;             const char* a3 = a2 + kstep; const char* b3 = b2 + kstep;
;             if (last && has_next) S.a_ready(nxt);
;             if constexpr (SP2) {
;             PG8_LDB(B0, 0, 0); PG8_LDB(B1, 0, 1); PG8_SCHED; PG8_LDA(At, 0, 0); PG8_STAGE(PG8_SA(1, 1), a1 + hstep, voffA);
;             PG8_WAIT_V(8); PG8_WAIT_L(0); PG8_BAR; PG8_MMA(0, 0, At, B0); PG8_MMA(0, 1, At, B1); PG8_BAR; PG8_SCHED;
;             PG8_LDA(At, 0, 1); PG8_STAGE(PG8_SB(0, 0), b2, voffB); PG8_STAGE(PG8_SB(0, 1), b2 + hstep, voffB); PG8_STAGE(PG8_SA(0, 0), a2, voffA);
;             PG8_WAIT_V(8); PG8_WAIT_L(0); PG8_BAR; PG8_MMA(1, 0, At, B0); PG8_MMA(1, 1, At, B1); PG8_BAR; PG8_SCHED;
.LBB0_2348:
	ds_read_b128 v[146:149], v152
	ds_read_b128 v[156:159], v152 offset:1024
	ds_read_b128 v[160:163], v152 offset:2048
	ds_read_b128 v[164:167], v152 offset:3072
	ds_read_b128 v[168:171], v153
	ds_read_b128 v[172:175], v153 offset:1024
	ds_read_b128 v[176:179], v153 offset:2048
	ds_read_b128 v[184:187], v153 offset:3072
	s_add_u32 s22, s44, 0xfffc0080
	s_addc_u32 s23, s45, -1
	s_cmp_eq_u32 s57, 12
	s_cselect_b32 s23, s19, s23
	s_cselect_b32 s22, s53, s22
	s_cselect_b32 s47, s17, s56
	s_cselect_b32 s46, s54, s55
	v_lshl_add_u64 v[180:181], s[44:45], 0, v[138:139]
	s_add_i32 m0, s31, 0xc000
	ds_read_b128 v[188:191], v154
	ds_read_b128 v[192:195], v154 offset:1024
	ds_read_b128 v[196:199], v154 offset:2048
	ds_read_b128 v[200:203], v154 offset:3072
	ds_read_b128 v[204:207], v154 offset:4096
	ds_read_b128 v[208:211], v154 offset:5120
	ds_read_b128 v[212:215], v154 offset:6144
	ds_read_b128 v[216:219], v154 offset:7168
	global_load_lds_dwordx4 v[180:181], off
	v_lshl_add_u64 v[180:181], s[44:45], 0, v[140:141]
	s_add_i32 m0, s31, 0xe000
	s_nop 0
	global_load_lds_dwordx4 v[180:181], off
	s_waitcnt vmcnt(8)
	s_waitcnt lgkmcnt(0)
	s_barrier
	s_waitcnt lgkmcnt(0)
	v_mfma_f32_16x16x32_bf16 v[126:129], v[146:149], v[188:191], v[126:129]
	v_mfma_f32_16x16x32_bf16 v[122:125], v[160:163], v[188:191], v[122:125]
	v_mfma_f32_16x16x32_bf16 v[110:113], v[146:149], v[196:199], v[110:113]
	v_mfma_f32_16x16x32_bf16 v[106:109], v[160:163], v[196:199], v[106:109]
	v_mfma_f32_16x16x32_bf16 v[94:97], v[146:149], v[204:207], v[94:97]
	v_mfma_f32_16x16x32_bf16 v[90:93], v[160:163], v[204:207], v[90:93]
	v_mfma_f32_16x16x32_bf16 v[78:81], v[146:149], v[212:215], v[78:81]
	v_mfma_f32_16x16x32_bf16 v[74:77], v[160:163], v[212:215], v[74:77]
	v_mfma_f32_16x16x32_bf16 v[126:129], v[156:159], v[192:195], v[126:129]
	v_mfma_f32_16x16x32_bf16 v[122:125], v[164:167], v[192:195], v[122:125]
	v_mfma_f32_16x16x32_bf16 v[110:113], v[156:159], v[200:203], v[110:113]
	v_mfma_f32_16x16x32_bf16 v[106:109], v[164:167], v[200:203], v[106:109]
	v_mfma_f32_16x16x32_bf16 v[94:97], v[156:159], v[208:211], v[94:97]
	v_mfma_f32_16x16x32_bf16 v[90:93], v[164:167], v[208:211], v[90:93]
	v_mfma_f32_16x16x32_bf16 v[78:81], v[156:159], v[216:219], v[78:81]
	v_mfma_f32_16x16x32_bf16 v[74:77], v[164:167], v[216:219], v[74:77]
	v_mfma_f32_16x16x32_bf16 v[118:121], v[168:171], v[188:191], v[118:121]
	v_mfma_f32_16x16x32_bf16 v[114:117], v[176:179], v[188:191], v[114:117]
	v_mfma_f32_16x16x32_bf16 v[102:105], v[168:171], v[196:199], v[102:105]
	v_mfma_f32_16x16x32_bf16 v[98:101], v[176:179], v[196:199], v[98:101]
	v_mfma_f32_16x16x32_bf16 v[86:89], v[168:171], v[204:207], v[86:89]
	v_mfma_f32_16x16x32_bf16 v[82:85], v[176:179], v[204:207], v[82:85]
	v_mfma_f32_16x16x32_bf16 v[70:73], v[168:171], v[212:215], v[70:73]
	v_mfma_f32_16x16x32_bf16 v[66:69], v[176:179], v[212:215], v[66:69]
	v_mfma_f32_16x16x32_bf16 v[118:121], v[172:175], v[192:195], v[118:121]
	v_mfma_f32_16x16x32_bf16 v[114:117], v[184:187], v[192:195], v[114:117]
	v_mfma_f32_16x16x32_bf16 v[102:105], v[172:175], v[200:203], v[102:105]
	v_mfma_f32_16x16x32_bf16 v[98:101], v[184:187], v[200:203], v[98:101]
	v_mfma_f32_16x16x32_bf16 v[86:89], v[172:175], v[208:211], v[86:89]
	v_mfma_f32_16x16x32_bf16 v[82:85], v[184:187], v[208:211], v[82:85]
	v_mfma_f32_16x16x32_bf16 v[70:73], v[172:175], v[216:219], v[70:73]
	v_mfma_f32_16x16x32_bf16 v[66:69], v[184:187], v[216:219], v[66:69]
	s_barrier
	s_add_i32 s58, s51, s30
	v_lshl_add_u64 v[180:181], s[46:47], 0, v[132:133]
	s_mov_b32 m0, s58
	ds_read_b128 v[188:191], v154 offset:16384
	ds_read_b128 v[192:195], v154 offset:17408
	ds_read_b128 v[196:199], v154 offset:18432
	ds_read_b128 v[200:203], v154 offset:19456
	ds_read_b128 v[204:207], v154 offset:20480
	ds_read_b128 v[208:211], v154 offset:21504
	ds_read_b128 v[212:215], v154 offset:22528
	ds_read_b128 v[216:219], v154 offset:23552
	global_load_lds_dwordx4 v[180:181], off
	s_add_i32 m0, s58, 0x2000
	s_add_u32 s58, s46, 0x40000
	v_lshl_add_u64 v[220:221], s[46:47], 0, v[136:137]
	s_addc_u32 s59, s47, 0
	s_add_i32 s60, s52, s30
	global_load_lds_dwordx4 v[220:221], off
	v_lshl_add_u64 v[222:223], s[58:59], 0, v[132:133]
	s_mov_b32 m0, s60
	v_lshl_add_u64 v[224:225], s[22:23], 0, v[134:135]
	global_load_lds_dwordx4 v[222:223], off
	v_lshl_add_u64 v[222:223], s[58:59], 0, v[136:137]
	s_add_i32 m0, s60, 0x2000
	s_nop 0
	global_load_lds_dwordx4 v[222:223], off
	v_lshl_add_u64 v[222:223], s[22:23], 0, v[130:131]
	s_mov_b32 m0, s31
	s_nop 0
	global_load_lds_dwordx4 v[222:223], off
	s_mov_b32 m0, s33
	s_nop 0
	global_load_lds_dwordx4 v[224:225], off
	s_waitcnt vmcnt(8)
	s_waitcnt lgkmcnt(0)
	s_barrier
; #define PG8_STAGE(bufoff, gbase, voff) do { _Pragma("unroll") for (int _i = 0; _i < 2; ++_i) \
;         __builtin_amdgcn_global_load_lds((const unsigned*)((const char*)(gbase) + (voff)[_i]), (PG8_LAS unsigned*)(lds + (bufoff) + ldsw + _i * 8192), 16, 0, 0); } while (0)
; #define PG8_LDA(dst, b, h) do { _Pragma("unroll") for (int m = 0; m < 4; ++m) _Pragma("unroll") for (int k = 0; k < 2; ++k) dst[m][k] = *(const PG8_LAS bf16x8*)(lds + PG8_SA(b, h) + aoff + m * 2048 + k * 1024); } while (0)
; #define PG8_LDB(dst, b, h) do { _Pragma("unroll") for (int n = 0; n < 2; ++n) _Pragma("unroll") for (int k = 0; k < 2; ++k) dst[n][k] = *(const PG8_LAS bf16x8*)(lds + PG8_SB(b, h) + boff + n * 2048 + k * 1024); } while (0)
; #define PG8_MMA(ai, bj, At, Bt) do { __builtin_amdgcn_s_setprio(1); _Pragma("unroll") for (int m = 0; m < 4; ++m) _Pragma("unroll") for (int n = 0; n < 2; ++n) _Pragma("unroll") for (int k = 0; k < 2; ++k) \
;         acc[ai][bj][m][n] = __builtin_amdgcn_mfma_f32_16x16x32_bf16(Bt[n][k], At[m][k], acc[ai][bj][m][n], 0, 0, 0); __builtin_amdgcn_s_setprio(0); } while (0)
; #define PG8_WAIT_V(n) asm volatile("s_waitcnt vmcnt(" #n ")" ::: "memory")
; #define PG8_WAIT_L(n) asm volatile("s_waitcnt lgkmcnt(" #n ")" ::: "memory")
; #define PG8_BAR __builtin_amdgcn_s_barrier()
; #define PG8_SCHED __builtin_amdgcn_sched_barrier(0)
; template <class Epi, class Sched, bool ALIGN_EPI = false, bool SP2 = false>
; __device__ __forceinline__ void gemm_phase(PG8_LAS unsigned char* lds, const Gemm g, const Sched& S, const Epi& E) {
;     ...
;             PG8_WAIT_V(8); PG8_WAIT_L(0); PG8_BAR; PG8_MMA(1, 0, At, B0); PG8_MMA(1, 1, At, B1); PG8_BAR; PG8_SCHED;
;             PG8_LDB(B0, 1, 0); PG8_LDB(B1, 1, 1); PG8_SCHED; PG8_LDA(At, 1, 0); PG8_STAGE(PG8_SA(0, 1), a2 + hstep, voffA);
;             PG8_WAIT_V(8); PG8_WAIT_L(0); PG8_BAR; PG8_MMA(0, 0, At, B0); PG8_MMA(0, 1, At, B1); PG8_BAR; PG8_SCHED;
	s_waitcnt lgkmcnt(0)
	v_mfma_f32_16x16x32_bf16 v[62:65], v[146:149], v[188:191], v[62:65]
	v_mfma_f32_16x16x32_bf16 v[58:61], v[160:163], v[188:191], v[58:61]
	v_mfma_f32_16x16x32_bf16 v[46:49], v[146:149], v[196:199], v[46:49]
	v_mfma_f32_16x16x32_bf16 v[42:45], v[160:163], v[196:199], v[42:45]
	v_mfma_f32_16x16x32_bf16 v[30:33], v[146:149], v[204:207], v[30:33]
	v_mfma_f32_16x16x32_bf16 v[26:29], v[160:163], v[204:207], v[26:29]
	v_mfma_f32_16x16x32_bf16 v[14:17], v[146:149], v[212:215], v[14:17]
	v_mfma_f32_16x16x32_bf16 v[10:13], v[160:163], v[212:215], v[10:13]
	v_mfma_f32_16x16x32_bf16 v[62:65], v[156:159], v[192:195], v[62:65]
	v_mfma_f32_16x16x32_bf16 v[58:61], v[164:167], v[192:195], v[58:61]
	v_mfma_f32_16x16x32_bf16 v[46:49], v[156:159], v[200:203], v[46:49]
	v_mfma_f32_16x16x32_bf16 v[42:45], v[164:167], v[200:203], v[42:45]
	v_mfma_f32_16x16x32_bf16 v[30:33], v[156:159], v[208:211], v[30:33]
	v_mfma_f32_16x16x32_bf16 v[26:29], v[164:167], v[208:211], v[26:29]
	v_mfma_f32_16x16x32_bf16 v[14:17], v[156:159], v[216:219], v[14:17]
	v_mfma_f32_16x16x32_bf16 v[10:13], v[164:167], v[216:219], v[10:13]
	v_mfma_f32_16x16x32_bf16 v[54:57], v[168:171], v[188:191], v[54:57]
	v_mfma_f32_16x16x32_bf16 v[50:53], v[176:179], v[188:191], v[50:53]
	v_mfma_f32_16x16x32_bf16 v[38:41], v[168:171], v[196:199], v[38:41]
	v_mfma_f32_16x16x32_bf16 v[34:37], v[176:179], v[196:199], v[34:37]
	v_mfma_f32_16x16x32_bf16 v[22:25], v[168:171], v[204:207], v[22:25]
	v_mfma_f32_16x16x32_bf16 v[18:21], v[176:179], v[204:207], v[18:21]
	v_mfma_f32_16x16x32_bf16 v[6:9], v[168:171], v[212:215], v[6:9]
	v_mfma_f32_16x16x32_bf16 v[2:5], v[176:179], v[212:215], v[2:5]
	v_mfma_f32_16x16x32_bf16 v[54:57], v[172:175], v[192:195], v[54:57]
	v_mfma_f32_16x16x32_bf16 v[50:53], v[184:187], v[192:195], v[50:53]
	v_mfma_f32_16x16x32_bf16 v[38:41], v[172:175], v[200:203], v[38:41]
	v_mfma_f32_16x16x32_bf16 v[34:37], v[184:187], v[200:203], v[34:37]
	v_mfma_f32_16x16x32_bf16 v[22:25], v[172:175], v[208:211], v[22:25]
	v_mfma_f32_16x16x32_bf16 v[18:21], v[184:187], v[208:211], v[18:21]
	v_mfma_f32_16x16x32_bf16 v[6:9], v[172:175], v[216:219], v[6:9]
	v_mfma_f32_16x16x32_bf16 v[2:5], v[184:187], v[216:219], v[2:5]
	s_barrier
	s_add_i32 s58, 0, 0x18000
	s_add_i32 s59, 0, 0x1c000
	v_add_u32_e32 v164, s58, v150
	v_add_u32_e32 v183, s59, v150
	ds_read_b128 v[146:149], v164
	ds_read_b128 v[156:159], v164 offset:1024
	ds_read_b128 v[160:163], v164 offset:2048
	ds_read_b128 v[164:167], v164 offset:3072
	ds_read_b128 v[168:171], v183
	ds_read_b128 v[172:175], v183 offset:1024
	ds_read_b128 v[176:179], v183 offset:2048
	ds_read_b128 v[184:187], v183 offset:3072
	s_add_u32 s22, s22, 0x40000
	s_addc_u32 s23, s23, 0
	s_mov_b32 m0, s34
	v_lshl_add_u64 v[226:227], s[22:23], 0, v[130:131]
	ds_read_b128 v[188:191], v154 offset:32768
	ds_read_b128 v[192:195], v154 offset:33792
	ds_read_b128 v[196:199], v154 offset:34816
	ds_read_b128 v[200:203], v154 offset:35840
	ds_read_b128 v[204:207], v154 offset:36864
	ds_read_b128 v[208:211], v154 offset:37888
	ds_read_b128 v[212:215], v154 offset:38912
	ds_read_b128 v[216:219], v154 offset:39936
	global_load_lds_dwordx4 v[226:227], off
	v_lshl_add_u64 v[226:227], s[22:23], 0, v[134:135]
	s_mov_b32 m0, s35
	s_nop 0
	global_load_lds_dwordx4 v[226:227], off
	s_waitcnt vmcnt(8)
	s_waitcnt lgkmcnt(0)
	s_barrier
	s_waitcnt lgkmcnt(0)
	v_mfma_f32_16x16x32_bf16 v[126:129], v[146:149], v[188:191], v[126:129]
	v_mfma_f32_16x16x32_bf16 v[122:125], v[160:163], v[188:191], v[122:125]
	v_mfma_f32_16x16x32_bf16 v[110:113], v[146:149], v[196:199], v[110:113]
	v_mfma_f32_16x16x32_bf16 v[106:109], v[160:163], v[196:199], v[106:109]
	v_mfma_f32_16x16x32_bf16 v[94:97], v[146:149], v[204:207], v[94:97]
	v_mfma_f32_16x16x32_bf16 v[90:93], v[160:163], v[204:207], v[90:93]
	v_mfma_f32_16x16x32_bf16 v[78:81], v[146:149], v[212:215], v[78:81]
	v_mfma_f32_16x16x32_bf16 v[74:77], v[160:163], v[212:215], v[74:77]
	v_mfma_f32_16x16x32_bf16 v[126:129], v[156:159], v[192:195], v[126:129]
	v_mfma_f32_16x16x32_bf16 v[122:125], v[164:167], v[192:195], v[122:125]
	v_mfma_f32_16x16x32_bf16 v[110:113], v[156:159], v[200:203], v[110:113]
	v_mfma_f32_16x16x32_bf16 v[106:109], v[164:167], v[200:203], v[106:109]
	v_mfma_f32_16x16x32_bf16 v[94:97], v[156:159], v[208:211], v[94:97]
	v_mfma_f32_16x16x32_bf16 v[90:93], v[164:167], v[208:211], v[90:93]
	v_mfma_f32_16x16x32_bf16 v[78:81], v[156:159], v[216:219], v[78:81]
	v_mfma_f32_16x16x32_bf16 v[74:77], v[164:167], v[216:219], v[74:77]
	v_mfma_f32_16x16x32_bf16 v[118:121], v[168:171], v[188:191], v[118:121]
	v_mfma_f32_16x16x32_bf16 v[114:117], v[176:179], v[188:191], v[114:117]
	v_mfma_f32_16x16x32_bf16 v[102:105], v[168:171], v[196:199], v[102:105]
	v_mfma_f32_16x16x32_bf16 v[98:101], v[176:179], v[196:199], v[98:101]
	v_mfma_f32_16x16x32_bf16 v[86:89], v[168:171], v[204:207], v[86:89]
	v_mfma_f32_16x16x32_bf16 v[82:85], v[176:179], v[204:207], v[82:85]
	v_mfma_f32_16x16x32_bf16 v[70:73], v[168:171], v[212:215], v[70:73]
	v_mfma_f32_16x16x32_bf16 v[66:69], v[176:179], v[212:215], v[66:69]
	v_mfma_f32_16x16x32_bf16 v[118:121], v[172:175], v[192:195], v[118:121]
	v_mfma_f32_16x16x32_bf16 v[114:117], v[184:187], v[192:195], v[114:117]
	v_mfma_f32_16x16x32_bf16 v[102:105], v[172:175], v[200:203], v[102:105]
	v_mfma_f32_16x16x32_bf16 v[98:101], v[184:187], v[200:203], v[98:101]
	v_mfma_f32_16x16x32_bf16 v[86:89], v[172:175], v[208:211], v[86:89]
	v_mfma_f32_16x16x32_bf16 v[82:85], v[184:187], v[208:211], v[82:85]
	v_mfma_f32_16x16x32_bf16 v[70:73], v[172:175], v[216:219], v[70:73]
	v_mfma_f32_16x16x32_bf16 v[66:69], v[184:187], v[216:219], v[66:69]
	s_barrier
; #define PG8_STAGE(bufoff, gbase, voff) do { _Pragma("unroll") for (int _i = 0; _i < 2; ++_i) \
;         __builtin_amdgcn_global_load_lds((const unsigned*)((const char*)(gbase) + (voff)[_i]), (PG8_LAS unsigned*)(lds + (bufoff) + ldsw + _i * 8192), 16, 0, 0); } while (0)
; #define PG8_LDA(dst, b, h) do { _Pragma("unroll") for (int m = 0; m < 4; ++m) _Pragma("unroll") for (int k = 0; k < 2; ++k) dst[m][k] = *(const PG8_LAS bf16x8*)(lds + PG8_SA(b, h) + aoff + m * 2048 + k * 1024); } while (0)
; #define PG8_MMA(ai, bj, At, Bt) do { __builtin_amdgcn_s_setprio(1); _Pragma("unroll") for (int m = 0; m < 4; ++m) _Pragma("unroll") for (int n = 0; n < 2; ++n) _Pragma("unroll") for (int k = 0; k < 2; ++k) \
;         acc[ai][bj][m][n] = __builtin_amdgcn_mfma_f32_16x16x32_bf16(Bt[n][k], At[m][k], acc[ai][bj][m][n], 0, 0, 0); __builtin_amdgcn_s_setprio(0); } while (0)
; #define PG8_WAIT_V(n) asm volatile("s_waitcnt vmcnt(" #n ")" ::: "memory")
; #define PG8_WAIT_L(n) asm volatile("s_waitcnt lgkmcnt(" #n ")" ::: "memory")
; #define PG8_BAR __builtin_amdgcn_s_barrier()
; #define PG8_SCHED __builtin_amdgcn_sched_barrier(0)
; template <class Epi, class Sched, bool ALIGN_EPI = false, bool SP2 = false>
; __device__ __forceinline__ void gemm_phase(PG8_LAS unsigned char* lds, const Gemm g, const Sched& S, const Epi& E) {
;     ...
;         for (int t = 0; t < nt; t += 2) {
;     ...
;             PG8_LDA(At, 1, 1); PG8_STAGE(PG8_SB(1, 0), b3, voffB); PG8_STAGE(PG8_SB(1, 1), b3 + hstep, voffB); PG8_STAGE(PG8_SA(1, 0), a3, voffA);
;             PG8_WAIT_V(8); PG8_WAIT_L(0); PG8_BAR; PG8_MMA(1, 0, At, B0); PG8_MMA(1, 1, At, B1); PG8_BAR; PG8_SCHED;
	s_add_i32 s22, s58, s30
	v_lshl_add_u64 v[180:181], v[180:181], 0, s[12:13]
	s_mov_b32 m0, s22
	ds_read_b128 v[188:191], v154 offset:49152
	ds_read_b128 v[192:195], v154 offset:50176
	ds_read_b128 v[196:199], v154 offset:51200
	ds_read_b128 v[200:203], v154 offset:52224
	ds_read_b128 v[204:207], v154 offset:53248
	ds_read_b128 v[208:211], v154 offset:54272
	ds_read_b128 v[212:215], v154 offset:55296
	ds_read_b128 v[216:219], v154 offset:56320
	global_load_lds_dwordx4 v[180:181], off
	s_add_i32 m0, s22, 0x2000
	s_add_u32 s22, s46, 0x40080
	v_lshl_add_u64 v[180:181], v[220:221], 0, s[12:13]
	s_addc_u32 s23, s47, 0
	s_add_i32 s46, s59, s30
	global_load_lds_dwordx4 v[180:181], off
	v_lshl_add_u64 v[180:181], s[22:23], 0, v[132:133]
	s_mov_b32 m0, s46
	s_nop 0
	global_load_lds_dwordx4 v[180:181], off
	v_lshl_add_u64 v[180:181], s[22:23], 0, v[136:137]
	s_add_i32 m0, s46, 0x2000
	s_nop 0
	global_load_lds_dwordx4 v[180:181], off
	v_lshl_add_u64 v[180:181], v[222:223], 0, s[12:13]
	s_mov_b32 m0, s43
	s_nop 0
	global_load_lds_dwordx4 v[180:181], off
	v_lshl_add_u64 v[180:181], v[224:225], 0, s[12:13]
	s_mov_b32 m0, s48
	s_nop 0
	global_load_lds_dwordx4 v[180:181], off
	s_waitcnt vmcnt(8)
	s_waitcnt lgkmcnt(0)
	s_barrier
	s_waitcnt lgkmcnt(0)
	v_mfma_f32_16x16x32_bf16 v[62:65], v[146:149], v[188:191], v[62:65]
	v_mfma_f32_16x16x32_bf16 v[58:61], v[160:163], v[188:191], v[58:61]
	v_mfma_f32_16x16x32_bf16 v[46:49], v[146:149], v[196:199], v[46:49]
	v_mfma_f32_16x16x32_bf16 v[42:45], v[160:163], v[196:199], v[42:45]
	v_mfma_f32_16x16x32_bf16 v[30:33], v[146:149], v[204:207], v[30:33]
	v_mfma_f32_16x16x32_bf16 v[26:29], v[160:163], v[204:207], v[26:29]
	v_mfma_f32_16x16x32_bf16 v[14:17], v[146:149], v[212:215], v[14:17]
	v_mfma_f32_16x16x32_bf16 v[10:13], v[160:163], v[212:215], v[10:13]
	v_mfma_f32_16x16x32_bf16 v[62:65], v[156:159], v[192:195], v[62:65]
	v_mfma_f32_16x16x32_bf16 v[58:61], v[164:167], v[192:195], v[58:61]
	v_mfma_f32_16x16x32_bf16 v[46:49], v[156:159], v[200:203], v[46:49]
	v_mfma_f32_16x16x32_bf16 v[42:45], v[164:167], v[200:203], v[42:45]
	v_mfma_f32_16x16x32_bf16 v[30:33], v[156:159], v[208:211], v[30:33]
	v_mfma_f32_16x16x32_bf16 v[26:29], v[164:167], v[208:211], v[26:29]
	v_mfma_f32_16x16x32_bf16 v[14:17], v[156:159], v[216:219], v[14:17]
	v_mfma_f32_16x16x32_bf16 v[10:13], v[164:167], v[216:219], v[10:13]
	v_mfma_f32_16x16x32_bf16 v[54:57], v[168:171], v[188:191], v[54:57]
	v_mfma_f32_16x16x32_bf16 v[50:53], v[176:179], v[188:191], v[50:53]
	v_mfma_f32_16x16x32_bf16 v[38:41], v[168:171], v[196:199], v[38:41]
	v_mfma_f32_16x16x32_bf16 v[34:37], v[176:179], v[196:199], v[34:37]
	v_mfma_f32_16x16x32_bf16 v[22:25], v[168:171], v[204:207], v[22:25]
	v_mfma_f32_16x16x32_bf16 v[18:21], v[176:179], v[204:207], v[18:21]
	v_mfma_f32_16x16x32_bf16 v[6:9], v[168:171], v[212:215], v[6:9]
	v_mfma_f32_16x16x32_bf16 v[2:5], v[176:179], v[212:215], v[2:5]
	v_mfma_f32_16x16x32_bf16 v[54:57], v[172:175], v[192:195], v[54:57]
	v_mfma_f32_16x16x32_bf16 v[50:53], v[184:187], v[192:195], v[50:53]
	v_mfma_f32_16x16x32_bf16 v[38:41], v[172:175], v[200:203], v[38:41]
	v_mfma_f32_16x16x32_bf16 v[34:37], v[184:187], v[200:203], v[34:37]
	v_mfma_f32_16x16x32_bf16 v[22:25], v[172:175], v[208:211], v[22:25]
	v_mfma_f32_16x16x32_bf16 v[18:21], v[184:187], v[208:211], v[18:21]
	v_mfma_f32_16x16x32_bf16 v[6:9], v[172:175], v[216:219], v[6:9]
	v_mfma_f32_16x16x32_bf16 v[2:5], v[184:187], v[216:219], v[2:5]
	s_barrier
	s_add_i32 s57, s57, 2
	s_add_u32 s44, s44, 0x100
	s_addc_u32 s45, s45, 0
	s_add_u32 s55, s55, 0x100
	s_addc_u32 s56, s56, 0
	s_cmp_gt_u32 s57, 13
	s_cbranch_scc0 .LBB0_2348
	s_and_b64 vcc, exec, s[14:15]
	s_cbranch_vccz .LBB0_2351
	s_barrier

; #define PG8_STAGE(bufoff, gbase, voff) do { _Pragma("unroll") for (int _i = 0; _i < 2; ++_i) \
;         __builtin_amdgcn_global_load_lds((const unsigned*)((const char*)(gbase) + (voff)[_i]), (PG8_LAS unsigned*)(lds + (bufoff) + ldsw + _i * 8192), 16, 0, 0); } while (0)
; #define PG8_LDA(dst, b, h) do { _Pragma("unroll") for (int m = 0; m < 4; ++m) _Pragma("unroll") for (int k = 0; k < 2; ++k) dst[m][k] = *(const PG8_LAS bf16x8*)(lds + PG8_SA(b, h) + aoff + m * 2048 + k * 1024); } while (0)
; #define PG8_LDB(dst, b, h) do { _Pragma("unroll") for (int n = 0; n < 2; ++n) _Pragma("unroll") for (int k = 0; k < 2; ++k) dst[n][k] = *(const PG8_LAS bf16x8*)(lds + PG8_SB(b, h) + boff + n * 2048 + k * 1024); } while (0)
; #define PG8_MMA(ai, bj, At, Bt) do { __builtin_amdgcn_s_setprio(1); _Pragma("unroll") for (int m = 0; m < 4; ++m) _Pragma("unroll") for (int n = 0; n < 2; ++n) _Pragma("unroll") for (int k = 0; k < 2; ++k) \
;         acc[ai][bj][m][n] = __builtin_amdgcn_mfma_f32_16x16x32_bf16(Bt[n][k], At[m][k], acc[ai][bj][m][n], 0, 0, 0); __builtin_amdgcn_s_setprio(0); } while (0)
; #define PG8_WAIT_V(n) asm volatile("s_waitcnt vmcnt(" #n ")" ::: "memory")
; #define PG8_BAR __builtin_amdgcn_s_barrier()
; template <class Epi, class Sched, bool ALIGN_EPI = false, bool SP2 = false>
; __device__ __forceinline__ void gemm_phase(PG8_LAS unsigned char* lds, const Gemm g, const Sched& S, const Epi& E) {
;     ...
;         for (int t = 0; t < nt; t += 2) {
;             const bool last = (t == nt - 2);
;             const char* a1 = cA + (size_t)(t + 1) * kstep;
;             const char* a2 = last ? nA : cA + (size_t)(t + 2) * kstep; const char* b2 = last ? nB : cB + (size_t)(t + 2) * kstep;
;             const char* a3 = a2 + kstep; const char* b3 = b2 + kstep;
;             if (last && has_next) S.a_ready(nxt);
;             if constexpr (SP2) {
;             PG8_LDB(B0, 0, 0); PG8_LDB(B1, 0, 1); PG8_SCHED; PG8_LDA(At, 0, 0); PG8_STAGE(PG8_SA(1, 1), a1 + hstep, voffA);
;             PG8_WAIT_V(8); PG8_WAIT_L(0); PG8_BAR; PG8_MMA(0, 0, At, B0); PG8_MMA(0, 1, At, B1); PG8_BAR; PG8_SCHED;
;             PG8_LDA(At, 0, 1); PG8_STAGE(PG8_SB(0, 0), b2, voffB); PG8_STAGE(PG8_SB(0, 1), b2 + hstep, voffB); PG8_STAGE(PG8_SA(0, 0), a2, voffA);
;             PG8_WAIT_V(8); PG8_WAIT_L(0); PG8_BAR; PG8_MMA(1, 0, At, B0); PG8_MMA(1, 1, At, B1); PG8_BAR; PG8_SCHED;
.LBB0_2439:
	ds_read_b128 v[146:149], v155
	ds_read_b128 v[160:163], v155 offset:1024
	ds_read_b128 v[164:167], v155 offset:2048
	ds_read_b128 v[168:171], v155 offset:3072
	ds_read_b128 v[172:175], v156
	ds_read_b128 v[176:179], v156 offset:1024
	ds_read_b128 v[184:187], v156 offset:2048
	ds_read_b128 v[188:191], v156 offset:3072
	s_add_u32 s22, s36, 0xfffc0080
	s_addc_u32 s23, s37, -1
	s_cmp_eq_u32 s52, 12
	s_cselect_b32 s23, s17, s23
	s_cselect_b32 s22, s48, s22
	s_cselect_b32 s39, s15, s51
	s_cselect_b32 s38, s49, s50
	v_lshl_add_u64 v[150:151], s[36:37], 0, v[138:139]
	s_add_i32 m0, s33, 0xc000
	ds_read_b128 v[192:195], v157
	ds_read_b128 v[196:199], v157 offset:1024
	ds_read_b128 v[200:203], v157 offset:2048
	ds_read_b128 v[204:207], v157 offset:3072
	ds_read_b128 v[208:211], v157 offset:4096
	ds_read_b128 v[212:215], v157 offset:5120
	ds_read_b128 v[216:219], v157 offset:6144
	ds_read_b128 v[220:223], v157 offset:7168
	global_load_lds_dwordx4 v[150:151], off
	v_lshl_add_u64 v[150:151], s[36:37], 0, v[140:141]
	s_add_i32 m0, s33, 0xe000
	s_nop 0
	global_load_lds_dwordx4 v[150:151], off
	s_waitcnt vmcnt(8)
	s_waitcnt lgkmcnt(0)
	s_barrier
	s_waitcnt lgkmcnt(0)
	v_mfma_f32_16x16x32_bf16 v[126:129], v[146:149], v[192:195], v[126:129]
	v_mfma_f32_16x16x32_bf16 v[122:125], v[164:167], v[192:195], v[122:125]
	v_mfma_f32_16x16x32_bf16 v[110:113], v[146:149], v[200:203], v[110:113]
	v_mfma_f32_16x16x32_bf16 v[106:109], v[164:167], v[200:203], v[106:109]
	v_mfma_f32_16x16x32_bf16 v[94:97], v[146:149], v[208:211], v[94:97]
	v_mfma_f32_16x16x32_bf16 v[90:93], v[164:167], v[208:211], v[90:93]
	v_mfma_f32_16x16x32_bf16 v[78:81], v[146:149], v[216:219], v[78:81]
	v_mfma_f32_16x16x32_bf16 v[74:77], v[164:167], v[216:219], v[74:77]
	v_mfma_f32_16x16x32_bf16 v[126:129], v[160:163], v[196:199], v[126:129]
	v_mfma_f32_16x16x32_bf16 v[122:125], v[168:171], v[196:199], v[122:125]
	v_mfma_f32_16x16x32_bf16 v[110:113], v[160:163], v[204:207], v[110:113]
	v_mfma_f32_16x16x32_bf16 v[106:109], v[168:171], v[204:207], v[106:109]
	v_mfma_f32_16x16x32_bf16 v[94:97], v[160:163], v[212:215], v[94:97]
	v_mfma_f32_16x16x32_bf16 v[90:93], v[168:171], v[212:215], v[90:93]
	v_mfma_f32_16x16x32_bf16 v[78:81], v[160:163], v[220:223], v[78:81]
	v_mfma_f32_16x16x32_bf16 v[74:77], v[168:171], v[220:223], v[74:77]
	v_mfma_f32_16x16x32_bf16 v[118:121], v[172:175], v[192:195], v[118:121]
	v_mfma_f32_16x16x32_bf16 v[114:117], v[184:187], v[192:195], v[114:117]
	v_mfma_f32_16x16x32_bf16 v[102:105], v[172:175], v[200:203], v[102:105]
	v_mfma_f32_16x16x32_bf16 v[98:101], v[184:187], v[200:203], v[98:101]
	v_mfma_f32_16x16x32_bf16 v[86:89], v[172:175], v[208:211], v[86:89]
	v_mfma_f32_16x16x32_bf16 v[82:85], v[184:187], v[208:211], v[82:85]
	v_mfma_f32_16x16x32_bf16 v[70:73], v[172:175], v[216:219], v[70:73]
	v_mfma_f32_16x16x32_bf16 v[66:69], v[184:187], v[216:219], v[66:69]
	v_mfma_f32_16x16x32_bf16 v[118:121], v[176:179], v[196:199], v[118:121]
	v_mfma_f32_16x16x32_bf16 v[114:117], v[188:191], v[196:199], v[114:117]
	v_mfma_f32_16x16x32_bf16 v[102:105], v[176:179], v[204:207], v[102:105]
	v_mfma_f32_16x16x32_bf16 v[98:101], v[188:191], v[204:207], v[98:101]
	v_mfma_f32_16x16x32_bf16 v[86:89], v[176:179], v[212:215], v[86:89]
	v_mfma_f32_16x16x32_bf16 v[82:85], v[188:191], v[212:215], v[82:85]
	v_mfma_f32_16x16x32_bf16 v[70:73], v[176:179], v[220:223], v[70:73]
	v_mfma_f32_16x16x32_bf16 v[66:69], v[188:191], v[220:223], v[66:69]
	s_barrier
	s_add_i32 s53, s45, s30
	v_lshl_add_u64 v[150:151], s[38:39], 0, v[132:133]
	s_mov_b32 m0, s53
	ds_read_b128 v[192:195], v157 offset:16384
	ds_read_b128 v[196:199], v157 offset:17408
	ds_read_b128 v[200:203], v157 offset:18432
	ds_read_b128 v[204:207], v157 offset:19456
	ds_read_b128 v[208:211], v157 offset:20480
	ds_read_b128 v[212:215], v157 offset:21504
	ds_read_b128 v[216:219], v157 offset:22528
	ds_read_b128 v[220:223], v157 offset:23552
	global_load_lds_dwordx4 v[150:151], off
	s_add_i32 m0, s53, 0x2000
	s_add_u32 s54, s38, 0x40000
	v_lshl_add_u64 v[180:181], s[38:39], 0, v[136:137]
	s_addc_u32 s55, s39, 0
	s_add_i32 s53, s46, s30
	global_load_lds_dwordx4 v[180:181], off
	v_lshl_add_u64 v[224:225], s[54:55], 0, v[132:133]
	s_mov_b32 m0, s53
	v_lshl_add_u64 v[226:227], s[22:23], 0, v[134:135]
	global_load_lds_dwordx4 v[224:225], off
	v_lshl_add_u64 v[224:225], s[54:55], 0, v[136:137]
	s_add_i32 m0, s53, 0x2000
	s_nop 0
	global_load_lds_dwordx4 v[224:225], off
	v_lshl_add_u64 v[224:225], s[22:23], 0, v[130:131]
	s_mov_b32 m0, s33
	s_nop 0
	global_load_lds_dwordx4 v[224:225], off
	s_mov_b32 m0, s34
	s_nop 0
	global_load_lds_dwordx4 v[226:227], off
	s_waitcnt vmcnt(8)
	s_waitcnt lgkmcnt(0)
	s_barrier
; #define PG8_STAGE(bufoff, gbase, voff) do { _Pragma("unroll") for (int _i = 0; _i < 2; ++_i) \
;         __builtin_amdgcn_global_load_lds((const unsigned*)((const char*)(gbase) + (voff)[_i]), (PG8_LAS unsigned*)(lds + (bufoff) + ldsw + _i * 8192), 16, 0, 0); } while (0)
; #define PG8_LDA(dst, b, h) do { _Pragma("unroll") for (int m = 0; m < 4; ++m) _Pragma("unroll") for (int k = 0; k < 2; ++k) dst[m][k] = *(const PG8_LAS bf16x8*)(lds + PG8_SA(b, h) + aoff + m * 2048 + k * 1024); } while (0)
; #define PG8_LDB(dst, b, h) do { _Pragma("unroll") for (int n = 0; n < 2; ++n) _Pragma("unroll") for (int k = 0; k < 2; ++k) dst[n][k] = *(const PG8_LAS bf16x8*)(lds + PG8_SB(b, h) + boff + n * 2048 + k * 1024); } while (0)
; #define PG8_MMA(ai, bj, At, Bt) do { __builtin_amdgcn_s_setprio(1); _Pragma("unroll") for (int m = 0; m < 4; ++m) _Pragma("unroll") for (int n = 0; n < 2; ++n) _Pragma("unroll") for (int k = 0; k < 2; ++k) \
;         acc[ai][bj][m][n] = __builtin_amdgcn_mfma_f32_16x16x32_bf16(Bt[n][k], At[m][k], acc[ai][bj][m][n], 0, 0, 0); __builtin_amdgcn_s_setprio(0); } while (0)
; #define PG8_WAIT_V(n) asm volatile("s_waitcnt vmcnt(" #n ")" ::: "memory")
; #define PG8_WAIT_L(n) asm volatile("s_waitcnt lgkmcnt(" #n ")" ::: "memory")
; #define PG8_BAR __builtin_amdgcn_s_barrier()
; #define PG8_SCHED __builtin_amdgcn_sched_barrier(0)
; template <class Epi, class Sched, bool ALIGN_EPI = false, bool SP2 = false>
; __device__ __forceinline__ void gemm_phase(PG8_LAS unsigned char* lds, const Gemm g, const Sched& S, const Epi& E) {
;     ...
;             PG8_WAIT_V(8); PG8_WAIT_L(0); PG8_BAR; PG8_MMA(1, 0, At, B0); PG8_MMA(1, 1, At, B1); PG8_BAR; PG8_SCHED;
;             PG8_LDB(B0, 1, 0); PG8_LDB(B1, 1, 1); PG8_SCHED; PG8_LDA(At, 1, 0); PG8_STAGE(PG8_SA(0, 1), a2 + hstep, voffA);
;             PG8_WAIT_V(8); PG8_WAIT_L(0); PG8_BAR; PG8_MMA(0, 0, At, B0); PG8_MMA(0, 1, At, B1); PG8_BAR; PG8_SCHED;
	s_waitcnt lgkmcnt(0)
	v_mfma_f32_16x16x32_bf16 v[62:65], v[146:149], v[192:195], v[62:65]
	v_mfma_f32_16x16x32_bf16 v[58:61], v[164:167], v[192:195], v[58:61]
	v_mfma_f32_16x16x32_bf16 v[46:49], v[146:149], v[200:203], v[46:49]
	v_mfma_f32_16x16x32_bf16 v[42:45], v[164:167], v[200:203], v[42:45]
	v_mfma_f32_16x16x32_bf16 v[30:33], v[146:149], v[208:211], v[30:33]
	v_mfma_f32_16x16x32_bf16 v[26:29], v[164:167], v[208:211], v[26:29]
	v_mfma_f32_16x16x32_bf16 v[14:17], v[146:149], v[216:219], v[14:17]
	v_mfma_f32_16x16x32_bf16 v[10:13], v[164:167], v[216:219], v[10:13]
	v_mfma_f32_16x16x32_bf16 v[62:65], v[160:163], v[196:199], v[62:65]
	v_mfma_f32_16x16x32_bf16 v[58:61], v[168:171], v[196:199], v[58:61]
	v_mfma_f32_16x16x32_bf16 v[46:49], v[160:163], v[204:207], v[46:49]
	v_mfma_f32_16x16x32_bf16 v[42:45], v[168:171], v[204:207], v[42:45]
	v_mfma_f32_16x16x32_bf16 v[30:33], v[160:163], v[212:215], v[30:33]
	v_mfma_f32_16x16x32_bf16 v[26:29], v[168:171], v[212:215], v[26:29]
	v_mfma_f32_16x16x32_bf16 v[14:17], v[160:163], v[220:223], v[14:17]
	v_mfma_f32_16x16x32_bf16 v[10:13], v[168:171], v[220:223], v[10:13]
	v_mfma_f32_16x16x32_bf16 v[54:57], v[172:175], v[192:195], v[54:57]
	v_mfma_f32_16x16x32_bf16 v[50:53], v[184:187], v[192:195], v[50:53]
	v_mfma_f32_16x16x32_bf16 v[38:41], v[172:175], v[200:203], v[38:41]
	v_mfma_f32_16x16x32_bf16 v[34:37], v[184:187], v[200:203], v[34:37]
	v_mfma_f32_16x16x32_bf16 v[22:25], v[172:175], v[208:211], v[22:25]
	v_mfma_f32_16x16x32_bf16 v[18:21], v[184:187], v[208:211], v[18:21]
	v_mfma_f32_16x16x32_bf16 v[6:9], v[172:175], v[216:219], v[6:9]
	v_mfma_f32_16x16x32_bf16 v[2:5], v[184:187], v[216:219], v[2:5]
	v_mfma_f32_16x16x32_bf16 v[54:57], v[176:179], v[196:199], v[54:57]
	v_mfma_f32_16x16x32_bf16 v[50:53], v[188:191], v[196:199], v[50:53]
	v_mfma_f32_16x16x32_bf16 v[38:41], v[176:179], v[204:207], v[38:41]
	v_mfma_f32_16x16x32_bf16 v[34:37], v[188:191], v[204:207], v[34:37]
	v_mfma_f32_16x16x32_bf16 v[22:25], v[176:179], v[212:215], v[22:25]
	v_mfma_f32_16x16x32_bf16 v[18:21], v[188:191], v[212:215], v[18:21]
	v_mfma_f32_16x16x32_bf16 v[6:9], v[176:179], v[220:223], v[6:9]
	v_mfma_f32_16x16x32_bf16 v[2:5], v[188:191], v[220:223], v[2:5]
	s_barrier
	s_add_i32 s53, 0, 0x18000
	v_add_u32_e32 v159, s53, v153
	s_add_i32 s54, 0, 0x1c000
	ds_read_b128 v[146:149], v159
	ds_read_b128 v[160:163], v159 offset:1024
	ds_read_b128 v[164:167], v159 offset:2048
	ds_read_b128 v[168:171], v159 offset:3072
	v_add_u32_e32 v159, s54, v153
	ds_read_b128 v[172:175], v159
	ds_read_b128 v[176:179], v159 offset:1024
	ds_read_b128 v[184:187], v159 offset:2048
	ds_read_b128 v[188:191], v159 offset:3072
	s_add_u32 s22, s22, 0x40000
	s_addc_u32 s23, s23, 0
	s_mov_b32 m0, s35
	v_lshl_add_u64 v[228:229], s[22:23], 0, v[130:131]
	ds_read_b128 v[192:195], v157 offset:32768
	ds_read_b128 v[196:199], v157 offset:33792
	ds_read_b128 v[200:203], v157 offset:34816
	ds_read_b128 v[204:207], v157 offset:35840
	ds_read_b128 v[208:211], v157 offset:36864
	ds_read_b128 v[212:215], v157 offset:37888
	ds_read_b128 v[216:219], v157 offset:38912
	ds_read_b128 v[220:223], v157 offset:39936
	global_load_lds_dwordx4 v[228:229], off
	v_lshl_add_u64 v[228:229], s[22:23], 0, v[134:135]
	s_mov_b32 m0, s40
	s_nop 0
	global_load_lds_dwordx4 v[228:229], off
	s_waitcnt vmcnt(8)
	s_waitcnt lgkmcnt(0)
	s_barrier
	s_waitcnt lgkmcnt(0)
	v_mfma_f32_16x16x32_bf16 v[126:129], v[146:149], v[192:195], v[126:129]
	v_mfma_f32_16x16x32_bf16 v[122:125], v[164:167], v[192:195], v[122:125]
	v_mfma_f32_16x16x32_bf16 v[110:113], v[146:149], v[200:203], v[110:113]
	v_mfma_f32_16x16x32_bf16 v[106:109], v[164:167], v[200:203], v[106:109]
	v_mfma_f32_16x16x32_bf16 v[94:97], v[146:149], v[208:211], v[94:97]
	v_mfma_f32_16x16x32_bf16 v[90:93], v[164:167], v[208:211], v[90:93]
	v_mfma_f32_16x16x32_bf16 v[78:81], v[146:149], v[216:219], v[78:81]
	v_mfma_f32_16x16x32_bf16 v[74:77], v[164:167], v[216:219], v[74:77]
	v_mfma_f32_16x16x32_bf16 v[126:129], v[160:163], v[196:199], v[126:129]
	v_mfma_f32_16x16x32_bf16 v[122:125], v[168:171], v[196:199], v[122:125]
	v_mfma_f32_16x16x32_bf16 v[110:113], v[160:163], v[204:207], v[110:113]
	v_mfma_f32_16x16x32_bf16 v[106:109], v[168:171], v[204:207], v[106:109]
	v_mfma_f32_16x16x32_bf16 v[94:97], v[160:163], v[212:215], v[94:97]
	v_mfma_f32_16x16x32_bf16 v[90:93], v[168:171], v[212:215], v[90:93]
	v_mfma_f32_16x16x32_bf16 v[78:81], v[160:163], v[220:223], v[78:81]
	v_mfma_f32_16x16x32_bf16 v[74:77], v[168:171], v[220:223], v[74:77]
	v_mfma_f32_16x16x32_bf16 v[118:121], v[172:175], v[192:195], v[118:121]
	v_mfma_f32_16x16x32_bf16 v[114:117], v[184:187], v[192:195], v[114:117]
	v_mfma_f32_16x16x32_bf16 v[102:105], v[172:175], v[200:203], v[102:105]
	v_mfma_f32_16x16x32_bf16 v[98:101], v[184:187], v[200:203], v[98:101]
	v_mfma_f32_16x16x32_bf16 v[86:89], v[172:175], v[208:211], v[86:89]
	v_mfma_f32_16x16x32_bf16 v[82:85], v[184:187], v[208:211], v[82:85]
	v_mfma_f32_16x16x32_bf16 v[70:73], v[172:175], v[216:219], v[70:73]
	v_mfma_f32_16x16x32_bf16 v[66:69], v[184:187], v[216:219], v[66:69]
	v_mfma_f32_16x16x32_bf16 v[118:121], v[176:179], v[196:199], v[118:121]
	v_mfma_f32_16x16x32_bf16 v[114:117], v[188:191], v[196:199], v[114:117]
	v_mfma_f32_16x16x32_bf16 v[102:105], v[176:179], v[204:207], v[102:105]
	v_mfma_f32_16x16x32_bf16 v[98:101], v[188:191], v[204:207], v[98:101]
	v_mfma_f32_16x16x32_bf16 v[86:89], v[176:179], v[212:215], v[86:89]
	v_mfma_f32_16x16x32_bf16 v[82:85], v[188:191], v[212:215], v[82:85]
	v_mfma_f32_16x16x32_bf16 v[70:73], v[176:179], v[220:223], v[70:73]
	v_mfma_f32_16x16x32_bf16 v[66:69], v[188:191], v[220:223], v[66:69]
	s_barrier
; #define PG8_STAGE(bufoff, gbase, voff) do { _Pragma("unroll") for (int _i = 0; _i < 2; ++_i) \
;         __builtin_amdgcn_global_load_lds((const unsigned*)((const char*)(gbase) + (voff)[_i]), (PG8_LAS unsigned*)(lds + (bufoff) + ldsw + _i * 8192), 16, 0, 0); } while (0)
; #define PG8_LDA(dst, b, h) do { _Pragma("unroll") for (int m = 0; m < 4; ++m) _Pragma("unroll") for (int k = 0; k < 2; ++k) dst[m][k] = *(const PG8_LAS bf16x8*)(lds + PG8_SA(b, h) + aoff + m * 2048 + k * 1024); } while (0)
; #define PG8_MMA(ai, bj, At, Bt) do { __builtin_amdgcn_s_setprio(1); _Pragma("unroll") for (int m = 0; m < 4; ++m) _Pragma("unroll") for (int n = 0; n < 2; ++n) _Pragma("unroll") for (int k = 0; k < 2; ++k) \
;         acc[ai][bj][m][n] = __builtin_amdgcn_mfma_f32_16x16x32_bf16(Bt[n][k], At[m][k], acc[ai][bj][m][n], 0, 0, 0); __builtin_amdgcn_s_setprio(0); } while (0)
; #define PG8_WAIT_V(n) asm volatile("s_waitcnt vmcnt(" #n ")" ::: "memory")
; #define PG8_WAIT_L(n) asm volatile("s_waitcnt lgkmcnt(" #n ")" ::: "memory")
; #define PG8_BAR __builtin_amdgcn_s_barrier()
; #define PG8_SCHED __builtin_amdgcn_sched_barrier(0)
; template <class Epi, class Sched, bool ALIGN_EPI = false, bool SP2 = false>
; __device__ __forceinline__ void gemm_phase(PG8_LAS unsigned char* lds, const Gemm g, const Sched& S, const Epi& E) {
;     ...
;         for (int t = 0; t < nt; t += 2) {
;     ...
;             PG8_LDA(At, 1, 1); PG8_STAGE(PG8_SB(1, 0), b3, voffB); PG8_STAGE(PG8_SB(1, 1), b3 + hstep, voffB); PG8_STAGE(PG8_SA(1, 0), a3, voffA);
;             PG8_WAIT_V(8); PG8_WAIT_L(0); PG8_BAR; PG8_MMA(1, 0, At, B0); PG8_MMA(1, 1, At, B1); PG8_BAR; PG8_SCHED;
	s_add_i32 s22, s53, s30
	v_lshl_add_u64 v[150:151], v[150:151], 0, s[10:11]
	s_mov_b32 m0, s22
	ds_read_b128 v[192:195], v157 offset:49152
	ds_read_b128 v[196:199], v157 offset:50176
	ds_read_b128 v[200:203], v157 offset:51200
	ds_read_b128 v[204:207], v157 offset:52224
	ds_read_b128 v[208:211], v157 offset:53248
	ds_read_b128 v[212:215], v157 offset:54272
	ds_read_b128 v[216:219], v157 offset:55296
	ds_read_b128 v[220:223], v157 offset:56320
	global_load_lds_dwordx4 v[150:151], off
	s_add_i32 m0, s22, 0x2000
	s_add_u32 s22, s38, 0x40080
	v_lshl_add_u64 v[150:151], v[180:181], 0, s[10:11]
	s_addc_u32 s23, s39, 0
	s_add_i32 s38, s54, s30
	global_load_lds_dwordx4 v[150:151], off
	v_lshl_add_u64 v[150:151], s[22:23], 0, v[132:133]
	s_mov_b32 m0, s38
	s_nop 0
	global_load_lds_dwordx4 v[150:151], off
	v_lshl_add_u64 v[150:151], s[22:23], 0, v[136:137]
	s_add_i32 m0, s38, 0x2000
	s_nop 0
	global_load_lds_dwordx4 v[150:151], off
	v_lshl_add_u64 v[150:151], v[224:225], 0, s[10:11]
	s_mov_b32 m0, s43
	s_nop 0
	global_load_lds_dwordx4 v[150:151], off
	v_lshl_add_u64 v[150:151], v[226:227], 0, s[10:11]
	s_mov_b32 m0, s44
	s_nop 0
	global_load_lds_dwordx4 v[150:151], off
	s_waitcnt vmcnt(8)
	s_waitcnt lgkmcnt(0)
	s_barrier
	s_waitcnt lgkmcnt(0)
	v_mfma_f32_16x16x32_bf16 v[62:65], v[146:149], v[192:195], v[62:65]
	v_mfma_f32_16x16x32_bf16 v[58:61], v[164:167], v[192:195], v[58:61]
	v_mfma_f32_16x16x32_bf16 v[46:49], v[146:149], v[200:203], v[46:49]
	v_mfma_f32_16x16x32_bf16 v[42:45], v[164:167], v[200:203], v[42:45]
	v_mfma_f32_16x16x32_bf16 v[30:33], v[146:149], v[208:211], v[30:33]
	v_mfma_f32_16x16x32_bf16 v[26:29], v[164:167], v[208:211], v[26:29]
	v_mfma_f32_16x16x32_bf16 v[14:17], v[146:149], v[216:219], v[14:17]
	v_mfma_f32_16x16x32_bf16 v[10:13], v[164:167], v[216:219], v[10:13]
	v_mfma_f32_16x16x32_bf16 v[62:65], v[160:163], v[196:199], v[62:65]
	v_mfma_f32_16x16x32_bf16 v[58:61], v[168:171], v[196:199], v[58:61]
	v_mfma_f32_16x16x32_bf16 v[46:49], v[160:163], v[204:207], v[46:49]
	v_mfma_f32_16x16x32_bf16 v[42:45], v[168:171], v[204:207], v[42:45]
	v_mfma_f32_16x16x32_bf16 v[30:33], v[160:163], v[212:215], v[30:33]
	v_mfma_f32_16x16x32_bf16 v[26:29], v[168:171], v[212:215], v[26:29]
	v_mfma_f32_16x16x32_bf16 v[14:17], v[160:163], v[220:223], v[14:17]
	v_mfma_f32_16x16x32_bf16 v[10:13], v[168:171], v[220:223], v[10:13]
	v_mfma_f32_16x16x32_bf16 v[54:57], v[172:175], v[192:195], v[54:57]
	v_mfma_f32_16x16x32_bf16 v[50:53], v[184:187], v[192:195], v[50:53]
	v_mfma_f32_16x16x32_bf16 v[38:41], v[172:175], v[200:203], v[38:41]
	v_mfma_f32_16x16x32_bf16 v[34:37], v[184:187], v[200:203], v[34:37]
	v_mfma_f32_16x16x32_bf16 v[22:25], v[172:175], v[208:211], v[22:25]
	v_mfma_f32_16x16x32_bf16 v[18:21], v[184:187], v[208:211], v[18:21]
	v_mfma_f32_16x16x32_bf16 v[6:9], v[172:175], v[216:219], v[6:9]
	v_mfma_f32_16x16x32_bf16 v[2:5], v[184:187], v[216:219], v[2:5]
	v_mfma_f32_16x16x32_bf16 v[54:57], v[176:179], v[196:199], v[54:57]
	v_mfma_f32_16x16x32_bf16 v[50:53], v[188:191], v[196:199], v[50:53]
	v_mfma_f32_16x16x32_bf16 v[38:41], v[176:179], v[204:207], v[38:41]
	v_mfma_f32_16x16x32_bf16 v[34:37], v[188:191], v[204:207], v[34:37]
	v_mfma_f32_16x16x32_bf16 v[22:25], v[176:179], v[212:215], v[22:25]
	v_mfma_f32_16x16x32_bf16 v[18:21], v[188:191], v[212:215], v[18:21]
	v_mfma_f32_16x16x32_bf16 v[6:9], v[176:179], v[220:223], v[6:9]
	v_mfma_f32_16x16x32_bf16 v[2:5], v[188:191], v[220:223], v[2:5]
	s_barrier
	s_add_i32 s52, s52, 2
	s_add_u32 s36, s36, 0x100
	s_addc_u32 s37, s37, 0
	s_add_u32 s50, s50, 0x100
	s_addc_u32 s51, s51, 0
	s_cmp_gt_u32 s52, 13
	s_cbranch_scc0 .LBB0_2439
	s_and_b64 vcc, exec, s[12:13]
	s_cbranch_vccz .LBB0_2442
	s_barrier

; #define PG8_STAGE(bufoff, gbase, voff) do { _Pragma("unroll") for (int _i = 0; _i < 2; ++_i) \
;         __builtin_amdgcn_global_load_lds((const unsigned*)((const char*)(gbase) + (voff)[_i]), (PG8_LAS unsigned*)(lds + (bufoff) + ldsw + _i * 8192), 16, 0, 0); } while (0)
; #define PG8_LDA(dst, b, h) do { _Pragma("unroll") for (int m = 0; m < 4; ++m) _Pragma("unroll") for (int k = 0; k < 2; ++k) dst[m][k] = *(const PG8_LAS bf16x8*)(lds + PG8_SA(b, h) + aoff + m * 2048 + k * 1024); } while (0)
; #define PG8_LDB(dst, b, h) do { _Pragma("unroll") for (int n = 0; n < 2; ++n) _Pragma("unroll") for (int k = 0; k < 2; ++k) dst[n][k] = *(const PG8_LAS bf16x8*)(lds + PG8_SB(b, h) + boff + n * 2048 + k * 1024); } while (0)
; #define PG8_MMA(ai, bj, At, Bt) do { __builtin_amdgcn_s_setprio(1); _Pragma("unroll") for (int m = 0; m < 4; ++m) _Pragma("unroll") for (int n = 0; n < 2; ++n) _Pragma("unroll") for (int k = 0; k < 2; ++k) \
;         acc[ai][bj][m][n] = __builtin_amdgcn_mfma_f32_16x16x32_bf16(Bt[n][k], At[m][k], acc[ai][bj][m][n], 0, 0, 0); __builtin_amdgcn_s_setprio(0); } while (0)
; #define PG8_WAIT_V(n) asm volatile("s_waitcnt vmcnt(" #n ")" ::: "memory")
; #define PG8_BAR __builtin_amdgcn_s_barrier()
; template <class Epi, class Sched, bool ALIGN_EPI = false, bool SP2 = false>
; __device__ __forceinline__ void gemm_phase(PG8_LAS unsigned char* lds, const Gemm g, const Sched& S, const Epi& E) {
;     ...
;         for (int t = 0; t < nt; t += 2) {
;             const bool last = (t == nt - 2);
;             const char* a1 = cA + (size_t)(t + 1) * kstep;
;             const char* a2 = last ? nA : cA + (size_t)(t + 2) * kstep; const char* b2 = last ? nB : cB + (size_t)(t + 2) * kstep;
;             const char* a3 = a2 + kstep; const char* b3 = b2 + kstep;
;             if (last && has_next) S.a_ready(nxt);
;             if constexpr (SP2) {
;             PG8_LDB(B0, 0, 0); PG8_LDB(B1, 0, 1); PG8_SCHED; PG8_LDA(At, 0, 0); PG8_STAGE(PG8_SA(1, 1), a1 + hstep, voffA);
;             PG8_WAIT_V(8); PG8_WAIT_L(0); PG8_BAR; PG8_MMA(0, 0, At, B0); PG8_MMA(0, 1, At, B1); PG8_BAR; PG8_SCHED;
;             PG8_LDA(At, 0, 1); PG8_STAGE(PG8_SB(0, 0), b2, voffB); PG8_STAGE(PG8_SB(0, 1), b2 + hstep, voffB); PG8_STAGE(PG8_SA(0, 0), a2, voffA);
;             PG8_WAIT_V(8); PG8_WAIT_L(0); PG8_BAR; PG8_MMA(1, 0, At, B0); PG8_MMA(1, 1, At, B1); PG8_BAR; PG8_SCHED;
.LBB0_2522:
	ds_read_b128 v[146:149], v152
	ds_read_b128 v[156:159], v152 offset:1024
	ds_read_b128 v[160:163], v152 offset:2048
	ds_read_b128 v[164:167], v152 offset:3072
	ds_read_b128 v[168:171], v153
	ds_read_b128 v[172:175], v153 offset:1024
	ds_read_b128 v[176:179], v153 offset:2048
	ds_read_b128 v[180:183], v153 offset:3072
	s_add_u32 s22, s42, 0xfffc0080
	s_addc_u32 s23, s43, -1
	s_cmp_eq_u32 s55, 12
	s_cselect_b32 s23, s19, s23
	s_cselect_b32 s22, s51, s22
	s_cselect_b32 s45, s17, s54
	s_cselect_b32 s44, s52, s53
	v_lshl_add_u64 v[216:217], s[42:43], 0, v[138:139]
	s_add_i32 m0, s31, 0xc000
	ds_read_b128 v[184:187], v154
	ds_read_b128 v[188:191], v154 offset:1024
	ds_read_b128 v[192:195], v154 offset:2048
	ds_read_b128 v[196:199], v154 offset:3072
	ds_read_b128 v[200:203], v154 offset:4096
	ds_read_b128 v[204:207], v154 offset:5120
	ds_read_b128 v[208:211], v154 offset:6144
	ds_read_b128 v[212:215], v154 offset:7168
	global_load_lds_dwordx4 v[216:217], off
	v_lshl_add_u64 v[216:217], s[42:43], 0, v[140:141]
	s_add_i32 m0, s31, 0xe000
	s_nop 0
	global_load_lds_dwordx4 v[216:217], off
	s_waitcnt vmcnt(8)
	s_waitcnt lgkmcnt(0)
	s_barrier
	s_waitcnt lgkmcnt(0)
	v_mfma_f32_16x16x32_bf16 v[126:129], v[146:149], v[184:187], v[126:129]
	v_mfma_f32_16x16x32_bf16 v[122:125], v[160:163], v[184:187], v[122:125]
	v_mfma_f32_16x16x32_bf16 v[110:113], v[146:149], v[192:195], v[110:113]
	v_mfma_f32_16x16x32_bf16 v[106:109], v[160:163], v[192:195], v[106:109]
	v_mfma_f32_16x16x32_bf16 v[94:97], v[146:149], v[200:203], v[94:97]
	v_mfma_f32_16x16x32_bf16 v[90:93], v[160:163], v[200:203], v[90:93]
	v_mfma_f32_16x16x32_bf16 v[78:81], v[146:149], v[208:211], v[78:81]
	v_mfma_f32_16x16x32_bf16 v[74:77], v[160:163], v[208:211], v[74:77]
	v_mfma_f32_16x16x32_bf16 v[126:129], v[156:159], v[188:191], v[126:129]
	v_mfma_f32_16x16x32_bf16 v[122:125], v[164:167], v[188:191], v[122:125]
	v_mfma_f32_16x16x32_bf16 v[110:113], v[156:159], v[196:199], v[110:113]
	v_mfma_f32_16x16x32_bf16 v[106:109], v[164:167], v[196:199], v[106:109]
	v_mfma_f32_16x16x32_bf16 v[94:97], v[156:159], v[204:207], v[94:97]
	v_mfma_f32_16x16x32_bf16 v[90:93], v[164:167], v[204:207], v[90:93]
	v_mfma_f32_16x16x32_bf16 v[78:81], v[156:159], v[212:215], v[78:81]
	v_mfma_f32_16x16x32_bf16 v[74:77], v[164:167], v[212:215], v[74:77]
	v_mfma_f32_16x16x32_bf16 v[118:121], v[168:171], v[184:187], v[118:121]
	v_mfma_f32_16x16x32_bf16 v[114:117], v[176:179], v[184:187], v[114:117]
	v_mfma_f32_16x16x32_bf16 v[102:105], v[168:171], v[192:195], v[102:105]
	v_mfma_f32_16x16x32_bf16 v[98:101], v[176:179], v[192:195], v[98:101]
	v_mfma_f32_16x16x32_bf16 v[86:89], v[168:171], v[200:203], v[86:89]
	v_mfma_f32_16x16x32_bf16 v[82:85], v[176:179], v[200:203], v[82:85]
	v_mfma_f32_16x16x32_bf16 v[70:73], v[168:171], v[208:211], v[70:73]
	v_mfma_f32_16x16x32_bf16 v[66:69], v[176:179], v[208:211], v[66:69]
	v_mfma_f32_16x16x32_bf16 v[118:121], v[172:175], v[188:191], v[118:121]
	v_mfma_f32_16x16x32_bf16 v[114:117], v[180:183], v[188:191], v[114:117]
	v_mfma_f32_16x16x32_bf16 v[102:105], v[172:175], v[196:199], v[102:105]
	v_mfma_f32_16x16x32_bf16 v[98:101], v[180:183], v[196:199], v[98:101]
	v_mfma_f32_16x16x32_bf16 v[86:89], v[172:175], v[204:207], v[86:89]
	v_mfma_f32_16x16x32_bf16 v[82:85], v[180:183], v[204:207], v[82:85]
	v_mfma_f32_16x16x32_bf16 v[70:73], v[172:175], v[212:215], v[70:73]
	v_mfma_f32_16x16x32_bf16 v[66:69], v[180:183], v[212:215], v[66:69]
	s_barrier
	s_add_i32 s56, s49, s30
	v_lshl_add_u64 v[216:217], s[44:45], 0, v[132:133]
	s_mov_b32 m0, s56
	ds_read_b128 v[184:187], v154 offset:16384
	ds_read_b128 v[188:191], v154 offset:17408
	ds_read_b128 v[192:195], v154 offset:18432
	ds_read_b128 v[196:199], v154 offset:19456
	ds_read_b128 v[200:203], v154 offset:20480
	ds_read_b128 v[204:207], v154 offset:21504
	ds_read_b128 v[208:211], v154 offset:22528
	ds_read_b128 v[212:215], v154 offset:23552
	global_load_lds_dwordx4 v[216:217], off
	s_add_i32 m0, s56, 0x2000
	s_add_u32 s56, s44, 0x40000
	v_lshl_add_u64 v[218:219], s[44:45], 0, v[136:137]
	s_addc_u32 s57, s45, 0
	s_add_i32 s58, s50, s30
	global_load_lds_dwordx4 v[218:219], off
	v_lshl_add_u64 v[220:221], s[56:57], 0, v[132:133]
	s_mov_b32 m0, s58
	v_lshl_add_u64 v[222:223], s[22:23], 0, v[134:135]
	global_load_lds_dwordx4 v[220:221], off
	v_lshl_add_u64 v[220:221], s[56:57], 0, v[136:137]
	s_add_i32 m0, s58, 0x2000
	s_nop 0
	global_load_lds_dwordx4 v[220:221], off
	v_lshl_add_u64 v[220:221], s[22:23], 0, v[130:131]
	s_mov_b32 m0, s31
	s_nop 0
	global_load_lds_dwordx4 v[220:221], off
	s_mov_b32 m0, s33
	s_nop 0
	global_load_lds_dwordx4 v[222:223], off
	s_waitcnt vmcnt(8)
	s_waitcnt lgkmcnt(0)
	s_barrier
; #define PG8_STAGE(bufoff, gbase, voff) do { _Pragma("unroll") for (int _i = 0; _i < 2; ++_i) \
;         __builtin_amdgcn_global_load_lds((const unsigned*)((const char*)(gbase) + (voff)[_i]), (PG8_LAS unsigned*)(lds + (bufoff) + ldsw + _i * 8192), 16, 0, 0); } while (0)
; #define PG8_LDA(dst, b, h) do { _Pragma("unroll") for (int m = 0; m < 4; ++m) _Pragma("unroll") for (int k = 0; k < 2; ++k) dst[m][k] = *(const PG8_LAS bf16x8*)(lds + PG8_SA(b, h) + aoff + m * 2048 + k * 1024); } while (0)
; #define PG8_LDB(dst, b, h) do { _Pragma("unroll") for (int n = 0; n < 2; ++n) _Pragma("unroll") for (int k = 0; k < 2; ++k) dst[n][k] = *(const PG8_LAS bf16x8*)(lds + PG8_SB(b, h) + boff + n * 2048 + k * 1024); } while (0)
; #define PG8_MMA(ai, bj, At, Bt) do { __builtin_amdgcn_s_setprio(1); _Pragma("unroll") for (int m = 0; m < 4; ++m) _Pragma("unroll") for (int n = 0; n < 2; ++n) _Pragma("unroll") for (int k = 0; k < 2; ++k) \
;         acc[ai][bj][m][n] = __builtin_amdgcn_mfma_f32_16x16x32_bf16(Bt[n][k], At[m][k], acc[ai][bj][m][n], 0, 0, 0); __builtin_amdgcn_s_setprio(0); } while (0)
; #define PG8_WAIT_V(n) asm volatile("s_waitcnt vmcnt(" #n ")" ::: "memory")
; #define PG8_WAIT_L(n) asm volatile("s_waitcnt lgkmcnt(" #n ")" ::: "memory")
; #define PG8_BAR __builtin_amdgcn_s_barrier()
; #define PG8_SCHED __builtin_amdgcn_sched_barrier(0)
; template <class Epi, class Sched, bool ALIGN_EPI = false, bool SP2 = false>
; __device__ __forceinline__ void gemm_phase(PG8_LAS unsigned char* lds, const Gemm g, const Sched& S, const Epi& E) {
;     ...
;             PG8_WAIT_V(8); PG8_WAIT_L(0); PG8_BAR; PG8_MMA(1, 0, At, B0); PG8_MMA(1, 1, At, B1); PG8_BAR; PG8_SCHED;
;             PG8_LDB(B0, 1, 0); PG8_LDB(B1, 1, 1); PG8_SCHED; PG8_LDA(At, 1, 0); PG8_STAGE(PG8_SA(0, 1), a2 + hstep, voffA);
;             PG8_WAIT_V(8); PG8_WAIT_L(0); PG8_BAR; PG8_MMA(0, 0, At, B0); PG8_MMA(0, 1, At, B1); PG8_BAR; PG8_SCHED;
	s_waitcnt lgkmcnt(0)
	v_mfma_f32_16x16x32_bf16 v[62:65], v[146:149], v[184:187], v[62:65]
	v_mfma_f32_16x16x32_bf16 v[58:61], v[160:163], v[184:187], v[58:61]
	v_mfma_f32_16x16x32_bf16 v[46:49], v[146:149], v[192:195], v[46:49]
	v_mfma_f32_16x16x32_bf16 v[42:45], v[160:163], v[192:195], v[42:45]
	v_mfma_f32_16x16x32_bf16 v[30:33], v[146:149], v[200:203], v[30:33]
	v_mfma_f32_16x16x32_bf16 v[26:29], v[160:163], v[200:203], v[26:29]
	v_mfma_f32_16x16x32_bf16 v[14:17], v[146:149], v[208:211], v[14:17]
	v_mfma_f32_16x16x32_bf16 v[10:13], v[160:163], v[208:211], v[10:13]
	v_mfma_f32_16x16x32_bf16 v[62:65], v[156:159], v[188:191], v[62:65]
	v_mfma_f32_16x16x32_bf16 v[58:61], v[164:167], v[188:191], v[58:61]
	v_mfma_f32_16x16x32_bf16 v[46:49], v[156:159], v[196:199], v[46:49]
	v_mfma_f32_16x16x32_bf16 v[42:45], v[164:167], v[196:199], v[42:45]
	v_mfma_f32_16x16x32_bf16 v[30:33], v[156:159], v[204:207], v[30:33]
	v_mfma_f32_16x16x32_bf16 v[26:29], v[164:167], v[204:207], v[26:29]
	v_mfma_f32_16x16x32_bf16 v[14:17], v[156:159], v[212:215], v[14:17]
	v_mfma_f32_16x16x32_bf16 v[10:13], v[164:167], v[212:215], v[10:13]
	v_mfma_f32_16x16x32_bf16 v[54:57], v[168:171], v[184:187], v[54:57]
	v_mfma_f32_16x16x32_bf16 v[50:53], v[176:179], v[184:187], v[50:53]
	v_mfma_f32_16x16x32_bf16 v[38:41], v[168:171], v[192:195], v[38:41]
	v_mfma_f32_16x16x32_bf16 v[34:37], v[176:179], v[192:195], v[34:37]
	v_mfma_f32_16x16x32_bf16 v[22:25], v[168:171], v[200:203], v[22:25]
	v_mfma_f32_16x16x32_bf16 v[18:21], v[176:179], v[200:203], v[18:21]
	v_mfma_f32_16x16x32_bf16 v[6:9], v[168:171], v[208:211], v[6:9]
	v_mfma_f32_16x16x32_bf16 v[2:5], v[176:179], v[208:211], v[2:5]
	v_mfma_f32_16x16x32_bf16 v[54:57], v[172:175], v[188:191], v[54:57]
	v_mfma_f32_16x16x32_bf16 v[50:53], v[180:183], v[188:191], v[50:53]
	v_mfma_f32_16x16x32_bf16 v[38:41], v[172:175], v[196:199], v[38:41]
	v_mfma_f32_16x16x32_bf16 v[34:37], v[180:183], v[196:199], v[34:37]
	v_mfma_f32_16x16x32_bf16 v[22:25], v[172:175], v[204:207], v[22:25]
	v_mfma_f32_16x16x32_bf16 v[18:21], v[180:183], v[204:207], v[18:21]
	v_mfma_f32_16x16x32_bf16 v[6:9], v[172:175], v[212:215], v[6:9]
	v_mfma_f32_16x16x32_bf16 v[2:5], v[180:183], v[212:215], v[2:5]
	s_barrier
	s_add_i32 s56, 0, 0x18000
	s_add_i32 s57, 0, 0x1c000
	v_add_u32_e32 v164, s56, v150
	v_add_u32_e32 v180, s57, v150
	ds_read_b128 v[146:149], v164
	ds_read_b128 v[156:159], v164 offset:1024
	ds_read_b128 v[160:163], v164 offset:2048
	ds_read_b128 v[164:167], v164 offset:3072
	ds_read_b128 v[168:171], v180
	ds_read_b128 v[172:175], v180 offset:1024
	ds_read_b128 v[176:179], v180 offset:2048
	ds_read_b128 v[180:183], v180 offset:3072
	s_add_u32 s22, s22, 0x40000
	s_addc_u32 s23, s23, 0
	s_mov_b32 m0, s34
	v_lshl_add_u64 v[224:225], s[22:23], 0, v[130:131]
	ds_read_b128 v[184:187], v154 offset:32768
	ds_read_b128 v[188:191], v154 offset:33792
	ds_read_b128 v[192:195], v154 offset:34816
	ds_read_b128 v[196:199], v154 offset:35840
	ds_read_b128 v[200:203], v154 offset:36864
	ds_read_b128 v[204:207], v154 offset:37888
	ds_read_b128 v[208:211], v154 offset:38912
	ds_read_b128 v[212:215], v154 offset:39936
	global_load_lds_dwordx4 v[224:225], off
	v_lshl_add_u64 v[224:225], s[22:23], 0, v[134:135]
	s_mov_b32 m0, s35
	s_nop 0
	global_load_lds_dwordx4 v[224:225], off
	s_waitcnt vmcnt(8)
	s_waitcnt lgkmcnt(0)
	s_barrier
	s_waitcnt lgkmcnt(0)
	v_mfma_f32_16x16x32_bf16 v[126:129], v[146:149], v[184:187], v[126:129]
	v_mfma_f32_16x16x32_bf16 v[122:125], v[160:163], v[184:187], v[122:125]
	v_mfma_f32_16x16x32_bf16 v[110:113], v[146:149], v[192:195], v[110:113]
	v_mfma_f32_16x16x32_bf16 v[106:109], v[160:163], v[192:195], v[106:109]
	v_mfma_f32_16x16x32_bf16 v[94:97], v[146:149], v[200:203], v[94:97]
	v_mfma_f32_16x16x32_bf16 v[90:93], v[160:163], v[200:203], v[90:93]
	v_mfma_f32_16x16x32_bf16 v[78:81], v[146:149], v[208:211], v[78:81]
	v_mfma_f32_16x16x32_bf16 v[74:77], v[160:163], v[208:211], v[74:77]
	v_mfma_f32_16x16x32_bf16 v[126:129], v[156:159], v[188:191], v[126:129]
	v_mfma_f32_16x16x32_bf16 v[122:125], v[164:167], v[188:191], v[122:125]
	v_mfma_f32_16x16x32_bf16 v[110:113], v[156:159], v[196:199], v[110:113]
	v_mfma_f32_16x16x32_bf16 v[106:109], v[164:167], v[196:199], v[106:109]
	v_mfma_f32_16x16x32_bf16 v[94:97], v[156:159], v[204:207], v[94:97]
	v_mfma_f32_16x16x32_bf16 v[90:93], v[164:167], v[204:207], v[90:93]
	v_mfma_f32_16x16x32_bf16 v[78:81], v[156:159], v[212:215], v[78:81]
	v_mfma_f32_16x16x32_bf16 v[74:77], v[164:167], v[212:215], v[74:77]
	v_mfma_f32_16x16x32_bf16 v[118:121], v[168:171], v[184:187], v[118:121]
	v_mfma_f32_16x16x32_bf16 v[114:117], v[176:179], v[184:187], v[114:117]
	v_mfma_f32_16x16x32_bf16 v[102:105], v[168:171], v[192:195], v[102:105]
	v_mfma_f32_16x16x32_bf16 v[98:101], v[176:179], v[192:195], v[98:101]
	v_mfma_f32_16x16x32_bf16 v[86:89], v[168:171], v[200:203], v[86:89]
	v_mfma_f32_16x16x32_bf16 v[82:85], v[176:179], v[200:203], v[82:85]
	v_mfma_f32_16x16x32_bf16 v[70:73], v[168:171], v[208:211], v[70:73]
	v_mfma_f32_16x16x32_bf16 v[66:69], v[176:179], v[208:211], v[66:69]
	v_mfma_f32_16x16x32_bf16 v[118:121], v[172:175], v[188:191], v[118:121]
	v_mfma_f32_16x16x32_bf16 v[114:117], v[180:183], v[188:191], v[114:117]
	v_mfma_f32_16x16x32_bf16 v[102:105], v[172:175], v[196:199], v[102:105]
	v_mfma_f32_16x16x32_bf16 v[98:101], v[180:183], v[196:199], v[98:101]
	v_mfma_f32_16x16x32_bf16 v[86:89], v[172:175], v[204:207], v[86:89]
	v_mfma_f32_16x16x32_bf16 v[82:85], v[180:183], v[204:207], v[82:85]
	v_mfma_f32_16x16x32_bf16 v[70:73], v[172:175], v[212:215], v[70:73]
	v_mfma_f32_16x16x32_bf16 v[66:69], v[180:183], v[212:215], v[66:69]
	s_barrier
; #define PG8_STAGE(bufoff, gbase, voff) do { _Pragma("unroll") for (int _i = 0; _i < 2; ++_i) \
;         __builtin_amdgcn_global_load_lds((const unsigned*)((const char*)(gbase) + (voff)[_i]), (PG8_LAS unsigned*)(lds + (bufoff) + ldsw + _i * 8192), 16, 0, 0); } while (0)
; #define PG8_LDA(dst, b, h) do { _Pragma("unroll") for (int m = 0; m < 4; ++m) _Pragma("unroll") for (int k = 0; k < 2; ++k) dst[m][k] = *(const PG8_LAS bf16x8*)(lds + PG8_SA(b, h) + aoff + m * 2048 + k * 1024); } while (0)
; #define PG8_MMA(ai, bj, At, Bt) do { __builtin_amdgcn_s_setprio(1); _Pragma("unroll") for (int m = 0; m < 4; ++m) _Pragma("unroll") for (int n = 0; n < 2; ++n) _Pragma("unroll") for (int k = 0; k < 2; ++k) \
;         acc[ai][bj][m][n] = __builtin_amdgcn_mfma_f32_16x16x32_bf16(Bt[n][k], At[m][k], acc[ai][bj][m][n], 0, 0, 0); __builtin_amdgcn_s_setprio(0); } while (0)
; #define PG8_WAIT_V(n) asm volatile("s_waitcnt vmcnt(" #n ")" ::: "memory")
; #define PG8_WAIT_L(n) asm volatile("s_waitcnt lgkmcnt(" #n ")" ::: "memory")
; #define PG8_BAR __builtin_amdgcn_s_barrier()
; #define PG8_SCHED __builtin_amdgcn_sched_barrier(0)
; template <class Epi, class Sched, bool ALIGN_EPI = false, bool SP2 = false>
; __device__ __forceinline__ void gemm_phase(PG8_LAS unsigned char* lds, const Gemm g, const Sched& S, const Epi& E) {
;     ...
;         for (int t = 0; t < nt; t += 2) {
;     ...
;             PG8_LDA(At, 1, 1); PG8_STAGE(PG8_SB(1, 0), b3, voffB); PG8_STAGE(PG8_SB(1, 1), b3 + hstep, voffB); PG8_STAGE(PG8_SA(1, 0), a3, voffA);
;             PG8_WAIT_V(8); PG8_WAIT_L(0); PG8_BAR; PG8_MMA(1, 0, At, B0); PG8_MMA(1, 1, At, B1); PG8_BAR; PG8_SCHED;
	s_add_i32 s22, s56, s30
	v_lshl_add_u64 v[216:217], v[216:217], 0, s[12:13]
	s_mov_b32 m0, s22
	ds_read_b128 v[184:187], v154 offset:49152
	ds_read_b128 v[188:191], v154 offset:50176
	ds_read_b128 v[192:195], v154 offset:51200
	ds_read_b128 v[196:199], v154 offset:52224
	ds_read_b128 v[200:203], v154 offset:53248
	ds_read_b128 v[204:207], v154 offset:54272
	ds_read_b128 v[208:211], v154 offset:55296
	ds_read_b128 v[212:215], v154 offset:56320
	global_load_lds_dwordx4 v[216:217], off
	s_add_i32 m0, s22, 0x2000
	s_add_u32 s22, s44, 0x40080
	v_lshl_add_u64 v[216:217], v[218:219], 0, s[12:13]
	s_addc_u32 s23, s45, 0
	s_add_i32 s44, s57, s30
	global_load_lds_dwordx4 v[216:217], off
	v_lshl_add_u64 v[216:217], s[22:23], 0, v[132:133]
	s_mov_b32 m0, s44
	s_nop 0
	global_load_lds_dwordx4 v[216:217], off
	v_lshl_add_u64 v[216:217], s[22:23], 0, v[136:137]
	s_add_i32 m0, s44, 0x2000
	s_nop 0
	global_load_lds_dwordx4 v[216:217], off
	v_lshl_add_u64 v[216:217], v[220:221], 0, s[12:13]
	s_mov_b32 m0, s41
	s_nop 0
	global_load_lds_dwordx4 v[216:217], off
	v_lshl_add_u64 v[216:217], v[222:223], 0, s[12:13]
	s_mov_b32 m0, s46
	s_nop 0
	global_load_lds_dwordx4 v[216:217], off
	s_waitcnt vmcnt(8)
	s_waitcnt lgkmcnt(0)
	s_barrier
	s_waitcnt lgkmcnt(0)
	v_mfma_f32_16x16x32_bf16 v[62:65], v[146:149], v[184:187], v[62:65]
	v_mfma_f32_16x16x32_bf16 v[58:61], v[160:163], v[184:187], v[58:61]
	v_mfma_f32_16x16x32_bf16 v[46:49], v[146:149], v[192:195], v[46:49]
	v_mfma_f32_16x16x32_bf16 v[42:45], v[160:163], v[192:195], v[42:45]
	v_mfma_f32_16x16x32_bf16 v[30:33], v[146:149], v[200:203], v[30:33]
	v_mfma_f32_16x16x32_bf16 v[26:29], v[160:163], v[200:203], v[26:29]
	v_mfma_f32_16x16x32_bf16 v[14:17], v[146:149], v[208:211], v[14:17]
	v_mfma_f32_16x16x32_bf16 v[10:13], v[160:163], v[208:211], v[10:13]
	v_mfma_f32_16x16x32_bf16 v[62:65], v[156:159], v[188:191], v[62:65]
	v_mfma_f32_16x16x32_bf16 v[58:61], v[164:167], v[188:191], v[58:61]
	v_mfma_f32_16x16x32_bf16 v[46:49], v[156:159], v[196:199], v[46:49]
	v_mfma_f32_16x16x32_bf16 v[42:45], v[164:167], v[196:199], v[42:45]
	v_mfma_f32_16x16x32_bf16 v[30:33], v[156:159], v[204:207], v[30:33]
	v_mfma_f32_16x16x32_bf16 v[26:29], v[164:167], v[204:207], v[26:29]
	v_mfma_f32_16x16x32_bf16 v[14:17], v[156:159], v[212:215], v[14:17]
	v_mfma_f32_16x16x32_bf16 v[10:13], v[164:167], v[212:215], v[10:13]
	v_mfma_f32_16x16x32_bf16 v[54:57], v[168:171], v[184:187], v[54:57]
	v_mfma_f32_16x16x32_bf16 v[50:53], v[176:179], v[184:187], v[50:53]
	v_mfma_f32_16x16x32_bf16 v[38:41], v[168:171], v[192:195], v[38:41]
	v_mfma_f32_16x16x32_bf16 v[34:37], v[176:179], v[192:195], v[34:37]
	v_mfma_f32_16x16x32_bf16 v[22:25], v[168:171], v[200:203], v[22:25]
	v_mfma_f32_16x16x32_bf16 v[18:21], v[176:179], v[200:203], v[18:21]
	v_mfma_f32_16x16x32_bf16 v[6:9], v[168:171], v[208:211], v[6:9]
	v_mfma_f32_16x16x32_bf16 v[2:5], v[176:179], v[208:211], v[2:5]
	v_mfma_f32_16x16x32_bf16 v[54:57], v[172:175], v[188:191], v[54:57]
	v_mfma_f32_16x16x32_bf16 v[50:53], v[180:183], v[188:191], v[50:53]
	v_mfma_f32_16x16x32_bf16 v[38:41], v[172:175], v[196:199], v[38:41]
	v_mfma_f32_16x16x32_bf16 v[34:37], v[180:183], v[196:199], v[34:37]
	v_mfma_f32_16x16x32_bf16 v[22:25], v[172:175], v[204:207], v[22:25]
	v_mfma_f32_16x16x32_bf16 v[18:21], v[180:183], v[204:207], v[18:21]
	v_mfma_f32_16x16x32_bf16 v[6:9], v[172:175], v[212:215], v[6:9]
	v_mfma_f32_16x16x32_bf16 v[2:5], v[180:183], v[212:215], v[2:5]
	s_barrier
	s_add_i32 s55, s55, 2
	s_add_u32 s42, s42, 0x100
	s_addc_u32 s43, s43, 0
	s_add_u32 s53, s53, 0x100
	s_addc_u32 s54, s54, 0
	s_cmp_gt_u32 s55, 13
	s_cbranch_scc0 .LBB0_2522
	s_and_b64 vcc, exec, s[14:15]
	s_cbranch_vccz .LBB0_2525
	s_barrier

; #define PG8_STAGE(bufoff, gbase, voff) do { _Pragma("unroll") for (int _i = 0; _i < 2; ++_i) \
;         __builtin_amdgcn_global_load_lds((const unsigned*)((const char*)(gbase) + (voff)[_i]), (PG8_LAS unsigned*)(lds + (bufoff) + ldsw + _i * 8192), 16, 0, 0); } while (0)
; #define PG8_LDA(dst, b, h) do { _Pragma("unroll") for (int m = 0; m < 4; ++m) _Pragma("unroll") for (int k = 0; k < 2; ++k) dst[m][k] = *(const PG8_LAS bf16x8*)(lds + PG8_SA(b, h) + aoff + m * 2048 + k * 1024); } while (0)
; #define PG8_LDB(dst, b, h) do { _Pragma("unroll") for (int n = 0; n < 2; ++n) _Pragma("unroll") for (int k = 0; k < 2; ++k) dst[n][k] = *(const PG8_LAS bf16x8*)(lds + PG8_SB(b, h) + boff + n * 2048 + k * 1024); } while (0)
; #define PG8_MMA(ai, bj, At, Bt) do { __builtin_amdgcn_s_setprio(1); _Pragma("unroll") for (int m = 0; m < 4; ++m) _Pragma("unroll") for (int n = 0; n < 2; ++n) _Pragma("unroll") for (int k = 0; k < 2; ++k) \
;         acc[ai][bj][m][n] = __builtin_amdgcn_mfma_f32_16x16x32_bf16(Bt[n][k], At[m][k], acc[ai][bj][m][n], 0, 0, 0); __builtin_amdgcn_s_setprio(0); } while (0)
; #define PG8_WAIT_V(n) asm volatile("s_waitcnt vmcnt(" #n ")" ::: "memory")
; #define PG8_BAR __builtin_amdgcn_s_barrier()
; template <class Epi, class Sched, bool ALIGN_EPI = false, bool SP2 = false>
; __device__ __forceinline__ void gemm_phase(PG8_LAS unsigned char* lds, const Gemm g, const Sched& S, const Epi& E) {
;     ...
;         for (int t = 0; t < nt; t += 2) {
;             const bool last = (t == nt - 2);
;             const char* a1 = cA + (size_t)(t + 1) * kstep;
;             const char* a2 = last ? nA : cA + (size_t)(t + 2) * kstep; const char* b2 = last ? nB : cB + (size_t)(t + 2) * kstep;
;             const char* a3 = a2 + kstep; const char* b3 = b2 + kstep;
;             if (last && has_next) S.a_ready(nxt);
;             if constexpr (SP2) {
;             PG8_LDB(B0, 0, 0); PG8_LDB(B1, 0, 1); PG8_SCHED; PG8_LDA(At, 0, 0); PG8_STAGE(PG8_SA(1, 1), a1 + hstep, voffA);
;             PG8_WAIT_V(8); PG8_WAIT_L(0); PG8_BAR; PG8_MMA(0, 0, At, B0); PG8_MMA(0, 1, At, B1); PG8_BAR; PG8_SCHED;
;             PG8_LDA(At, 0, 1); PG8_STAGE(PG8_SB(0, 0), b2, voffB); PG8_STAGE(PG8_SB(0, 1), b2 + hstep, voffB); PG8_STAGE(PG8_SA(0, 0), a2, voffA);
;             PG8_WAIT_V(8); PG8_WAIT_L(0); PG8_BAR; PG8_MMA(1, 0, At, B0); PG8_MMA(1, 1, At, B1); PG8_BAR; PG8_SCHED;
.LBB0_2613:
	ds_read_b128 v[144:147], v151
	ds_read_b128 v[156:159], v151 offset:1024
	ds_read_b128 v[160:163], v151 offset:2048
	ds_read_b128 v[164:167], v151 offset:3072
	ds_read_b128 v[168:171], v152
	ds_read_b128 v[172:175], v152 offset:1024
	ds_read_b128 v[176:179], v152 offset:2048
	ds_read_b128 v[180:183], v152 offset:3072
	s_add_u32 s22, s48, 0xfffc0080
	s_addc_u32 s23, s49, -1
	s_cmp_eq_u32 s66, 12
	s_cselect_b32 s23, s43, s23
	s_cselect_b32 s22, s62, s22
	s_cselect_b32 s51, s41, s65
	s_cselect_b32 s50, s63, s64
	v_lshl_add_u64 v[216:217], s[48:49], 0, v[136:137]
	s_add_i32 m0, s30, 0xc000
	ds_read_b128 v[184:187], v153
	ds_read_b128 v[188:191], v153 offset:1024
	ds_read_b128 v[192:195], v153 offset:2048
	ds_read_b128 v[196:199], v153 offset:3072
	ds_read_b128 v[200:203], v153 offset:4096
	ds_read_b128 v[204:207], v153 offset:5120
	ds_read_b128 v[208:211], v153 offset:6144
	ds_read_b128 v[212:215], v153 offset:7168
	global_load_lds_dwordx4 v[216:217], off
	v_lshl_add_u64 v[216:217], s[48:49], 0, v[138:139]
	s_add_i32 m0, s30, 0xe000
	s_nop 0
	global_load_lds_dwordx4 v[216:217], off
	s_waitcnt vmcnt(8)
	s_waitcnt lgkmcnt(0)
	s_barrier
	s_waitcnt lgkmcnt(0)
	v_mfma_f32_16x16x32_bf16 v[124:127], v[144:147], v[184:187], v[124:127]
	v_mfma_f32_16x16x32_bf16 v[120:123], v[160:163], v[184:187], v[120:123]
	v_mfma_f32_16x16x32_bf16 v[108:111], v[144:147], v[192:195], v[108:111]
	v_mfma_f32_16x16x32_bf16 v[104:107], v[160:163], v[192:195], v[104:107]
	v_mfma_f32_16x16x32_bf16 v[92:95], v[144:147], v[200:203], v[92:95]
	v_mfma_f32_16x16x32_bf16 v[88:91], v[160:163], v[200:203], v[88:91]
	v_mfma_f32_16x16x32_bf16 v[76:79], v[144:147], v[208:211], v[76:79]
	v_mfma_f32_16x16x32_bf16 v[72:75], v[160:163], v[208:211], v[72:75]
	v_mfma_f32_16x16x32_bf16 v[124:127], v[156:159], v[188:191], v[124:127]
	v_mfma_f32_16x16x32_bf16 v[120:123], v[164:167], v[188:191], v[120:123]
	v_mfma_f32_16x16x32_bf16 v[108:111], v[156:159], v[196:199], v[108:111]
	v_mfma_f32_16x16x32_bf16 v[104:107], v[164:167], v[196:199], v[104:107]
	v_mfma_f32_16x16x32_bf16 v[92:95], v[156:159], v[204:207], v[92:95]
	v_mfma_f32_16x16x32_bf16 v[88:91], v[164:167], v[204:207], v[88:91]
	v_mfma_f32_16x16x32_bf16 v[76:79], v[156:159], v[212:215], v[76:79]
	v_mfma_f32_16x16x32_bf16 v[72:75], v[164:167], v[212:215], v[72:75]
	v_mfma_f32_16x16x32_bf16 v[116:119], v[168:171], v[184:187], v[116:119]
	v_mfma_f32_16x16x32_bf16 v[112:115], v[176:179], v[184:187], v[112:115]
	v_mfma_f32_16x16x32_bf16 v[100:103], v[168:171], v[192:195], v[100:103]
	v_mfma_f32_16x16x32_bf16 v[96:99], v[176:179], v[192:195], v[96:99]
	v_mfma_f32_16x16x32_bf16 v[84:87], v[168:171], v[200:203], v[84:87]
	v_mfma_f32_16x16x32_bf16 v[80:83], v[176:179], v[200:203], v[80:83]
	v_mfma_f32_16x16x32_bf16 v[68:71], v[168:171], v[208:211], v[68:71]
	v_mfma_f32_16x16x32_bf16 v[64:67], v[176:179], v[208:211], v[64:67]
	v_mfma_f32_16x16x32_bf16 v[116:119], v[172:175], v[188:191], v[116:119]
	v_mfma_f32_16x16x32_bf16 v[112:115], v[180:183], v[188:191], v[112:115]
	v_mfma_f32_16x16x32_bf16 v[100:103], v[172:175], v[196:199], v[100:103]
	v_mfma_f32_16x16x32_bf16 v[96:99], v[180:183], v[196:199], v[96:99]
	v_mfma_f32_16x16x32_bf16 v[84:87], v[172:175], v[204:207], v[84:87]
	v_mfma_f32_16x16x32_bf16 v[80:83], v[180:183], v[204:207], v[80:83]
	v_mfma_f32_16x16x32_bf16 v[68:71], v[172:175], v[212:215], v[68:71]
	v_mfma_f32_16x16x32_bf16 v[64:67], v[180:183], v[212:215], v[64:67]
	s_barrier
	s_add_i32 s67, s55, s28
	v_lshl_add_u64 v[216:217], s[50:51], 0, v[130:131]
	s_mov_b32 m0, s67
	ds_read_b128 v[184:187], v153 offset:16384
	ds_read_b128 v[188:191], v153 offset:17408
	ds_read_b128 v[192:195], v153 offset:18432
	ds_read_b128 v[196:199], v153 offset:19456
	ds_read_b128 v[200:203], v153 offset:20480
	ds_read_b128 v[204:207], v153 offset:21504
	ds_read_b128 v[208:211], v153 offset:22528
	ds_read_b128 v[212:215], v153 offset:23552
	global_load_lds_dwordx4 v[216:217], off
	s_add_i32 m0, s67, 0x2000
	s_add_u32 s68, s50, 0x40000
	v_lshl_add_u64 v[218:219], s[50:51], 0, v[134:135]
	s_addc_u32 s69, s51, 0
	s_add_i32 s67, s56, s28
	global_load_lds_dwordx4 v[218:219], off
	v_lshl_add_u64 v[220:221], s[68:69], 0, v[130:131]
	s_mov_b32 m0, s67
	v_lshl_add_u64 v[222:223], s[22:23], 0, v[132:133]
	global_load_lds_dwordx4 v[220:221], off
	v_lshl_add_u64 v[220:221], s[68:69], 0, v[134:135]
	s_add_i32 m0, s67, 0x2000
	s_nop 0
	global_load_lds_dwordx4 v[220:221], off
	v_lshl_add_u64 v[220:221], s[22:23], 0, v[128:129]
	s_mov_b32 m0, s30
	s_nop 0
	global_load_lds_dwordx4 v[220:221], off
	s_mov_b32 m0, s31
	s_nop 0
	global_load_lds_dwordx4 v[222:223], off
	s_waitcnt vmcnt(8)
	s_waitcnt lgkmcnt(0)
	s_barrier
; #define PG8_STAGE(bufoff, gbase, voff) do { _Pragma("unroll") for (int _i = 0; _i < 2; ++_i) \
;         __builtin_amdgcn_global_load_lds((const unsigned*)((const char*)(gbase) + (voff)[_i]), (PG8_LAS unsigned*)(lds + (bufoff) + ldsw + _i * 8192), 16, 0, 0); } while (0)
; #define PG8_LDA(dst, b, h) do { _Pragma("unroll") for (int m = 0; m < 4; ++m) _Pragma("unroll") for (int k = 0; k < 2; ++k) dst[m][k] = *(const PG8_LAS bf16x8*)(lds + PG8_SA(b, h) + aoff + m * 2048 + k * 1024); } while (0)
; #define PG8_LDB(dst, b, h) do { _Pragma("unroll") for (int n = 0; n < 2; ++n) _Pragma("unroll") for (int k = 0; k < 2; ++k) dst[n][k] = *(const PG8_LAS bf16x8*)(lds + PG8_SB(b, h) + boff + n * 2048 + k * 1024); } while (0)
; #define PG8_MMA(ai, bj, At, Bt) do { __builtin_amdgcn_s_setprio(1); _Pragma("unroll") for (int m = 0; m < 4; ++m) _Pragma("unroll") for (int n = 0; n < 2; ++n) _Pragma("unroll") for (int k = 0; k < 2; ++k) \
;         acc[ai][bj][m][n] = __builtin_amdgcn_mfma_f32_16x16x32_bf16(Bt[n][k], At[m][k], acc[ai][bj][m][n], 0, 0, 0); __builtin_amdgcn_s_setprio(0); } while (0)
; #define PG8_WAIT_V(n) asm volatile("s_waitcnt vmcnt(" #n ")" ::: "memory")
; #define PG8_WAIT_L(n) asm volatile("s_waitcnt lgkmcnt(" #n ")" ::: "memory")
; #define PG8_BAR __builtin_amdgcn_s_barrier()
; #define PG8_SCHED __builtin_amdgcn_sched_barrier(0)
; template <class Epi, class Sched, bool ALIGN_EPI = false, bool SP2 = false>
; __device__ __forceinline__ void gemm_phase(PG8_LAS unsigned char* lds, const Gemm g, const Sched& S, const Epi& E) {
;     ...
;             PG8_WAIT_V(8); PG8_WAIT_L(0); PG8_BAR; PG8_MMA(1, 0, At, B0); PG8_MMA(1, 1, At, B1); PG8_BAR; PG8_SCHED;
;             PG8_LDB(B0, 1, 0); PG8_LDB(B1, 1, 1); PG8_SCHED; PG8_LDA(At, 1, 0); PG8_STAGE(PG8_SA(0, 1), a2 + hstep, voffA);
;             PG8_WAIT_V(8); PG8_WAIT_L(0); PG8_BAR; PG8_MMA(0, 0, At, B0); PG8_MMA(0, 1, At, B1); PG8_BAR; PG8_SCHED;
	s_waitcnt lgkmcnt(0)
	v_mfma_f32_16x16x32_bf16 v[60:63], v[144:147], v[184:187], v[60:63]
	v_mfma_f32_16x16x32_bf16 v[56:59], v[160:163], v[184:187], v[56:59]
	v_mfma_f32_16x16x32_bf16 v[44:47], v[144:147], v[192:195], v[44:47]
	v_mfma_f32_16x16x32_bf16 v[40:43], v[160:163], v[192:195], v[40:43]
	v_mfma_f32_16x16x32_bf16 v[28:31], v[144:147], v[200:203], v[28:31]
	v_mfma_f32_16x16x32_bf16 v[24:27], v[160:163], v[200:203], v[24:27]
	v_mfma_f32_16x16x32_bf16 v[12:15], v[144:147], v[208:211], v[12:15]
	v_mfma_f32_16x16x32_bf16 v[8:11], v[160:163], v[208:211], v[8:11]
	v_mfma_f32_16x16x32_bf16 v[60:63], v[156:159], v[188:191], v[60:63]
	v_mfma_f32_16x16x32_bf16 v[56:59], v[164:167], v[188:191], v[56:59]
	v_mfma_f32_16x16x32_bf16 v[44:47], v[156:159], v[196:199], v[44:47]
	v_mfma_f32_16x16x32_bf16 v[40:43], v[164:167], v[196:199], v[40:43]
	v_mfma_f32_16x16x32_bf16 v[28:31], v[156:159], v[204:207], v[28:31]
	v_mfma_f32_16x16x32_bf16 v[24:27], v[164:167], v[204:207], v[24:27]
	v_mfma_f32_16x16x32_bf16 v[12:15], v[156:159], v[212:215], v[12:15]
	v_mfma_f32_16x16x32_bf16 v[8:11], v[164:167], v[212:215], v[8:11]
	v_mfma_f32_16x16x32_bf16 v[52:55], v[168:171], v[184:187], v[52:55]
	v_mfma_f32_16x16x32_bf16 v[48:51], v[176:179], v[184:187], v[48:51]
	v_mfma_f32_16x16x32_bf16 v[36:39], v[168:171], v[192:195], v[36:39]
	v_mfma_f32_16x16x32_bf16 v[32:35], v[176:179], v[192:195], v[32:35]
	v_mfma_f32_16x16x32_bf16 v[20:23], v[168:171], v[200:203], v[20:23]
	v_mfma_f32_16x16x32_bf16 v[16:19], v[176:179], v[200:203], v[16:19]
	v_mfma_f32_16x16x32_bf16 v[4:7], v[168:171], v[208:211], v[4:7]
	v_mfma_f32_16x16x32_bf16 v[0:3], v[176:179], v[208:211], v[0:3]
	v_mfma_f32_16x16x32_bf16 v[52:55], v[172:175], v[188:191], v[52:55]
	v_mfma_f32_16x16x32_bf16 v[48:51], v[180:183], v[188:191], v[48:51]
	v_mfma_f32_16x16x32_bf16 v[36:39], v[172:175], v[196:199], v[36:39]
	v_mfma_f32_16x16x32_bf16 v[32:35], v[180:183], v[196:199], v[32:35]
	v_mfma_f32_16x16x32_bf16 v[20:23], v[172:175], v[204:207], v[20:23]
	v_mfma_f32_16x16x32_bf16 v[16:19], v[180:183], v[204:207], v[16:19]
	v_mfma_f32_16x16x32_bf16 v[4:7], v[172:175], v[212:215], v[4:7]
	v_mfma_f32_16x16x32_bf16 v[0:3], v[180:183], v[212:215], v[0:3]
	s_barrier
	s_add_i32 s67, 0, 0x18000
	v_add_u32_e32 v155, s67, v149
	s_add_i32 s68, 0, 0x1c000
	ds_read_b128 v[144:147], v155
	ds_read_b128 v[156:159], v155 offset:1024
	ds_read_b128 v[160:163], v155 offset:2048
	ds_read_b128 v[164:167], v155 offset:3072
	v_add_u32_e32 v155, s68, v149
	ds_read_b128 v[168:171], v155
	ds_read_b128 v[172:175], v155 offset:1024
	ds_read_b128 v[176:179], v155 offset:2048
	ds_read_b128 v[180:183], v155 offset:3072
	s_add_u32 s22, s22, 0x40000
	s_addc_u32 s23, s23, 0
	s_mov_b32 m0, s33
	v_lshl_add_u64 v[224:225], s[22:23], 0, v[128:129]
	ds_read_b128 v[184:187], v153 offset:32768
	ds_read_b128 v[188:191], v153 offset:33792
	ds_read_b128 v[192:195], v153 offset:34816
	ds_read_b128 v[196:199], v153 offset:35840
	ds_read_b128 v[200:203], v153 offset:36864
	ds_read_b128 v[204:207], v153 offset:37888
	ds_read_b128 v[208:211], v153 offset:38912
	ds_read_b128 v[212:215], v153 offset:39936
	global_load_lds_dwordx4 v[224:225], off
	v_lshl_add_u64 v[224:225], s[22:23], 0, v[132:133]
	s_mov_b32 m0, s34
	s_nop 0
	global_load_lds_dwordx4 v[224:225], off
	s_waitcnt vmcnt(8)
	s_waitcnt lgkmcnt(0)
	s_barrier
	s_waitcnt lgkmcnt(0)
	v_mfma_f32_16x16x32_bf16 v[124:127], v[144:147], v[184:187], v[124:127]
	v_mfma_f32_16x16x32_bf16 v[120:123], v[160:163], v[184:187], v[120:123]
	v_mfma_f32_16x16x32_bf16 v[108:111], v[144:147], v[192:195], v[108:111]
	v_mfma_f32_16x16x32_bf16 v[104:107], v[160:163], v[192:195], v[104:107]
	v_mfma_f32_16x16x32_bf16 v[92:95], v[144:147], v[200:203], v[92:95]
	v_mfma_f32_16x16x32_bf16 v[88:91], v[160:163], v[200:203], v[88:91]
	v_mfma_f32_16x16x32_bf16 v[76:79], v[144:147], v[208:211], v[76:79]
	v_mfma_f32_16x16x32_bf16 v[72:75], v[160:163], v[208:211], v[72:75]
	v_mfma_f32_16x16x32_bf16 v[124:127], v[156:159], v[188:191], v[124:127]
	v_mfma_f32_16x16x32_bf16 v[120:123], v[164:167], v[188:191], v[120:123]
	v_mfma_f32_16x16x32_bf16 v[108:111], v[156:159], v[196:199], v[108:111]
	v_mfma_f32_16x16x32_bf16 v[104:107], v[164:167], v[196:199], v[104:107]
	v_mfma_f32_16x16x32_bf16 v[92:95], v[156:159], v[204:207], v[92:95]
	v_mfma_f32_16x16x32_bf16 v[88:91], v[164:167], v[204:207], v[88:91]
	v_mfma_f32_16x16x32_bf16 v[76:79], v[156:159], v[212:215], v[76:79]
	v_mfma_f32_16x16x32_bf16 v[72:75], v[164:167], v[212:215], v[72:75]
	v_mfma_f32_16x16x32_bf16 v[116:119], v[168:171], v[184:187], v[116:119]
	v_mfma_f32_16x16x32_bf16 v[112:115], v[176:179], v[184:187], v[112:115]
	v_mfma_f32_16x16x32_bf16 v[100:103], v[168:171], v[192:195], v[100:103]
	v_mfma_f32_16x16x32_bf16 v[96:99], v[176:179], v[192:195], v[96:99]
	v_mfma_f32_16x16x32_bf16 v[84:87], v[168:171], v[200:203], v[84:87]
	v_mfma_f32_16x16x32_bf16 v[80:83], v[176:179], v[200:203], v[80:83]
	v_mfma_f32_16x16x32_bf16 v[68:71], v[168:171], v[208:211], v[68:71]
	v_mfma_f32_16x16x32_bf16 v[64:67], v[176:179], v[208:211], v[64:67]
	v_mfma_f32_16x16x32_bf16 v[116:119], v[172:175], v[188:191], v[116:119]
	v_mfma_f32_16x16x32_bf16 v[112:115], v[180:183], v[188:191], v[112:115]
	v_mfma_f32_16x16x32_bf16 v[100:103], v[172:175], v[196:199], v[100:103]
	v_mfma_f32_16x16x32_bf16 v[96:99], v[180:183], v[196:199], v[96:99]
	v_mfma_f32_16x16x32_bf16 v[84:87], v[172:175], v[204:207], v[84:87]
	v_mfma_f32_16x16x32_bf16 v[80:83], v[180:183], v[204:207], v[80:83]
	v_mfma_f32_16x16x32_bf16 v[68:71], v[172:175], v[212:215], v[68:71]
	v_mfma_f32_16x16x32_bf16 v[64:67], v[180:183], v[212:215], v[64:67]
	s_barrier
; #define PG8_STAGE(bufoff, gbase, voff) do { _Pragma("unroll") for (int _i = 0; _i < 2; ++_i) \
;         __builtin_amdgcn_global_load_lds((const unsigned*)((const char*)(gbase) + (voff)[_i]), (PG8_LAS unsigned*)(lds + (bufoff) + ldsw + _i * 8192), 16, 0, 0); } while (0)
; #define PG8_LDA(dst, b, h) do { _Pragma("unroll") for (int m = 0; m < 4; ++m) _Pragma("unroll") for (int k = 0; k < 2; ++k) dst[m][k] = *(const PG8_LAS bf16x8*)(lds + PG8_SA(b, h) + aoff + m * 2048 + k * 1024); } while (0)
; #define PG8_MMA(ai, bj, At, Bt) do { __builtin_amdgcn_s_setprio(1); _Pragma("unroll") for (int m = 0; m < 4; ++m) _Pragma("unroll") for (int n = 0; n < 2; ++n) _Pragma("unroll") for (int k = 0; k < 2; ++k) \
;         acc[ai][bj][m][n] = __builtin_amdgcn_mfma_f32_16x16x32_bf16(Bt[n][k], At[m][k], acc[ai][bj][m][n], 0, 0, 0); __builtin_amdgcn_s_setprio(0); } while (0)
; #define PG8_WAIT_V(n) asm volatile("s_waitcnt vmcnt(" #n ")" ::: "memory")
; #define PG8_WAIT_L(n) asm volatile("s_waitcnt lgkmcnt(" #n ")" ::: "memory")
; #define PG8_BAR __builtin_amdgcn_s_barrier()
; #define PG8_SCHED __builtin_amdgcn_sched_barrier(0)
; template <class Epi, class Sched, bool ALIGN_EPI = false, bool SP2 = false>
; __device__ __forceinline__ void gemm_phase(PG8_LAS unsigned char* lds, const Gemm g, const Sched& S, const Epi& E) {
;     ...
;         for (int t = 0; t < nt; t += 2) {
;     ...
;             PG8_LDA(At, 1, 1); PG8_STAGE(PG8_SB(1, 0), b3, voffB); PG8_STAGE(PG8_SB(1, 1), b3 + hstep, voffB); PG8_STAGE(PG8_SA(1, 0), a3, voffA);
;             PG8_WAIT_V(8); PG8_WAIT_L(0); PG8_BAR; PG8_MMA(1, 0, At, B0); PG8_MMA(1, 1, At, B1); PG8_BAR; PG8_SCHED;
	s_add_i32 s22, s67, s28
	v_lshl_add_u64 v[216:217], v[216:217], 0, s[14:15]
	s_mov_b32 m0, s22
	ds_read_b128 v[184:187], v153 offset:49152
	ds_read_b128 v[188:191], v153 offset:50176
	ds_read_b128 v[192:195], v153 offset:51200
	ds_read_b128 v[196:199], v153 offset:52224
	ds_read_b128 v[200:203], v153 offset:53248
	ds_read_b128 v[204:207], v153 offset:54272
	ds_read_b128 v[208:211], v153 offset:55296
	ds_read_b128 v[212:215], v153 offset:56320
	global_load_lds_dwordx4 v[216:217], off
	s_add_i32 m0, s22, 0x2000
	s_add_u32 s22, s50, 0x40080
	v_lshl_add_u64 v[216:217], v[218:219], 0, s[14:15]
	s_addc_u32 s23, s51, 0
	s_add_i32 s50, s68, s28
	global_load_lds_dwordx4 v[216:217], off
	v_lshl_add_u64 v[216:217], s[22:23], 0, v[130:131]
	s_mov_b32 m0, s50
	s_nop 0
	global_load_lds_dwordx4 v[216:217], off
	v_lshl_add_u64 v[216:217], s[22:23], 0, v[134:135]
	s_add_i32 m0, s50, 0x2000
	s_nop 0
	global_load_lds_dwordx4 v[216:217], off
	v_lshl_add_u64 v[216:217], v[220:221], 0, s[14:15]
	s_mov_b32 m0, s53
	s_nop 0
	global_load_lds_dwordx4 v[216:217], off
	v_lshl_add_u64 v[216:217], v[222:223], 0, s[14:15]
	s_mov_b32 m0, s54
	s_nop 0
	global_load_lds_dwordx4 v[216:217], off
	s_waitcnt vmcnt(8)
	s_waitcnt lgkmcnt(0)
	s_barrier
	s_waitcnt lgkmcnt(0)
	v_mfma_f32_16x16x32_bf16 v[60:63], v[144:147], v[184:187], v[60:63]
	v_mfma_f32_16x16x32_bf16 v[56:59], v[160:163], v[184:187], v[56:59]
	v_mfma_f32_16x16x32_bf16 v[44:47], v[144:147], v[192:195], v[44:47]
	v_mfma_f32_16x16x32_bf16 v[40:43], v[160:163], v[192:195], v[40:43]
	v_mfma_f32_16x16x32_bf16 v[28:31], v[144:147], v[200:203], v[28:31]
	v_mfma_f32_16x16x32_bf16 v[24:27], v[160:163], v[200:203], v[24:27]
	v_mfma_f32_16x16x32_bf16 v[12:15], v[144:147], v[208:211], v[12:15]
	v_mfma_f32_16x16x32_bf16 v[8:11], v[160:163], v[208:211], v[8:11]
	v_mfma_f32_16x16x32_bf16 v[60:63], v[156:159], v[188:191], v[60:63]
	v_mfma_f32_16x16x32_bf16 v[56:59], v[164:167], v[188:191], v[56:59]
	v_mfma_f32_16x16x32_bf16 v[44:47], v[156:159], v[196:199], v[44:47]
	v_mfma_f32_16x16x32_bf16 v[40:43], v[164:167], v[196:199], v[40:43]
	v_mfma_f32_16x16x32_bf16 v[28:31], v[156:159], v[204:207], v[28:31]
	v_mfma_f32_16x16x32_bf16 v[24:27], v[164:167], v[204:207], v[24:27]
	v_mfma_f32_16x16x32_bf16 v[12:15], v[156:159], v[212:215], v[12:15]
	v_mfma_f32_16x16x32_bf16 v[8:11], v[164:167], v[212:215], v[8:11]
	v_mfma_f32_16x16x32_bf16 v[52:55], v[168:171], v[184:187], v[52:55]
	v_mfma_f32_16x16x32_bf16 v[48:51], v[176:179], v[184:187], v[48:51]
	v_mfma_f32_16x16x32_bf16 v[36:39], v[168:171], v[192:195], v[36:39]
	v_mfma_f32_16x16x32_bf16 v[32:35], v[176:179], v[192:195], v[32:35]
	v_mfma_f32_16x16x32_bf16 v[20:23], v[168:171], v[200:203], v[20:23]
	v_mfma_f32_16x16x32_bf16 v[16:19], v[176:179], v[200:203], v[16:19]
	v_mfma_f32_16x16x32_bf16 v[4:7], v[168:171], v[208:211], v[4:7]
	v_mfma_f32_16x16x32_bf16 v[0:3], v[176:179], v[208:211], v[0:3]
	v_mfma_f32_16x16x32_bf16 v[52:55], v[172:175], v[188:191], v[52:55]
	v_mfma_f32_16x16x32_bf16 v[48:51], v[180:183], v[188:191], v[48:51]
	v_mfma_f32_16x16x32_bf16 v[36:39], v[172:175], v[196:199], v[36:39]
	v_mfma_f32_16x16x32_bf16 v[32:35], v[180:183], v[196:199], v[32:35]
	v_mfma_f32_16x16x32_bf16 v[20:23], v[172:175], v[204:207], v[20:23]
	v_mfma_f32_16x16x32_bf16 v[16:19], v[180:183], v[204:207], v[16:19]
	v_mfma_f32_16x16x32_bf16 v[4:7], v[172:175], v[212:215], v[4:7]
	v_mfma_f32_16x16x32_bf16 v[0:3], v[180:183], v[212:215], v[0:3]
	s_barrier
	s_add_i32 s66, s66, 2
	s_add_u32 s48, s48, 0x100
	s_addc_u32 s49, s49, 0
	s_add_u32 s64, s64, 0x100
	s_addc_u32 s65, s65, 0
	s_cmp_gt_u32 s66, 13
	s_cbranch_scc0 .LBB0_2613
	s_and_b64 vcc, exec, s[16:17]
	s_cbranch_vccz .LBB0_2616
	s_barrier
